# baseline (speedup 1.0000x reference)
_Z12k1_colsum_q8PKfPjPfS2_:
	s_load_dwordx8 s[4:11], s[0:1], 0x0
	v_and_b32_e32 v1, 63, v0
	v_lshrrev_b32_e32 v41, 6, v0
	s_mul_i32 s12, s2, 0xc35
	s_lshr_b32 s12, s12, 4
	v_readfirstlane_b32 s14, v41
	s_add_i32 s13, s2, 1
	s_mul_i32 s13, s13, 0xc35
	s_lshr_b32 s13, s13, 4
	s_sub_u32 s13, s13, s12
	s_sub_u32 s15, s13, 0xc0
	s_cmp_lt_u32 s14, s15
	s_cselect_b32 s29, 1, 0
	v_lshlrev_b32_e32 v34, 4, v1
	v_min_u32_e32 v35, 57, v1
	v_lshlrev_b32_e32 v35, 4, v35
	v_cmp_gt_u32_e64 s[18:19], 58, v1
	s_lshl_b32 s35, s14, 13
	s_add_u32 s36, s35, 0x1000
	v_add_u32_e32 v38, s35, v34
	v_lshrrev_b32_e32 v41, 5, v1
	v_mov_b32_e32 v42, 0xc35000
	v_mul_lo_u32 v39, v41, v42
	v_and_b32_e32 v42, 31, v1
	v_lshl_add_u32 v39, v42, 2, v39
	v_mov_b32_e32 v2, 0
	v_mov_b32_e32 v3, 0
	v_mov_b32_e32 v4, 0
	v_mov_b32_e32 v5, 0
	v_mov_b32_e32 v6, 0
	v_mov_b32_e32 v7, 0
	v_mov_b32_e32 v8, 0
	v_mov_b32_e32 v9, 0
	v_mov_b32_e32 v10, 0
	v_mov_b32_e32 v11, 0
	v_mov_b32_e32 v12, 0
	v_mov_b32_e32 v13, 0
	v_mov_b32_e32 v14, 0
	v_mov_b32_e32 v15, 0
	v_mov_b32_e32 v16, 0
	v_mov_b32_e32 v17, 0
	v_mov_b32_e32 v40, 0
	v_mov_b32_e32 v47, 0x42fe0000
	s_mov_b32 s32, 0x42fe0000
	s_mov_b32 s33, 0xc0c0400
	s_mov_b32 s34, 0x4000c0c
	s_add_u32 s15, s12, s14
	s_mul_i32 s37, s15, 0xfa0
	s_lshl_b32 s15, s15, 7
	s_waitcnt lgkmcnt(0)
	s_add_u32 s16, s4, s37
	s_addc_u32 s17, s5, 0
	s_add_u32 s40, s6, s15
	s_addc_u32 s41, s7, 0
	s_add_u32 s20, s40, 0
	s_addc_u32 s21, s41, 0
	s_add_u32 s22, s20, 0x186a000
	s_addc_u32 s23, s21, 0
	s_add_u32 s24, s22, 0x186a000
	s_addc_u32 s25, s23, 0
	s_add_u32 s26, s24, 0x186a000
	s_addc_u32 s27, s25, 0
	s_mov_b32 m0, s35
	s_nop 0
	global_load_lds_dwordx4 v34, s[16:17] sc1 nt
	global_load_lds_dwordx4 v34, s[16:17] offset:1024 sc1 nt
	global_load_lds_dwordx4 v34, s[16:17] offset:2048 sc1 nt
	global_load_lds_dwordx4 v35, s[16:17] offset:3072 sc1 nt
	s_add_u32 s16, s16, 0x7d00
	s_addc_u32 s17, s17, 0
	s_waitcnt vmcnt(0)
	ds_read_b128 v[18:21], v38 offset:0
	ds_read_b128 v[22:25], v38 offset:1024
	ds_read_b128 v[26:29], v38 offset:2048
	ds_read_b128 v[30:33], v38 offset:3072
	s_waitcnt lgkmcnt(0)
	s_mov_b32 m0, s36
	s_nop 0
	global_load_lds_dwordx4 v34, s[16:17] sc1 nt
	global_load_lds_dwordx4 v34, s[16:17] offset:1024 sc1 nt
	global_load_lds_dwordx4 v34, s[16:17] offset:2048 sc1 nt
	global_load_lds_dwordx4 v35, s[16:17] offset:3072 sc1 nt
	s_add_u32 s16, s16, 0x7d00
	s_addc_u32 s17, s17, 0
	v_cndmask_b32_e64 v30, 0, v30, s[18:19]
	v_cndmask_b32_e64 v31, 0, v31, s[18:19]
	v_cndmask_b32_e64 v32, 0, v32, s[18:19]
	v_cndmask_b32_e64 v33, 0, v33, s[18:19]
	v_max3_f32 v41, |v18|, |v19|, |v20|
	v_max3_f32 v42, |v21|, |v22|, |v23|
	v_max3_f32 v43, |v24|, |v25|, |v26|
	v_max3_f32 v44, |v27|, |v28|, |v29|
	v_max3_f32 v48, |v30|, |v31|, |v32|
	v_max3_f32 v41, v41, v42, |v33|
	v_max3_f32 v43, v43, v44, v48
	v_max_f32_e32 v41, v41, v43
	v_pk_add_f32 v[2:3], v[2:3], v[18:19]
	v_pk_add_f32 v[4:5], v[4:5], v[20:21]
	v_max_f32_dpp v41, v41, v41 quad_perm:[1,0,3,2] row_mask:0xf bank_mask:0xf
	v_pk_add_f32 v[6:7], v[6:7], v[22:23]
	v_pk_add_f32 v[8:9], v[8:9], v[24:25]
	v_max_f32_dpp v41, v41, v41 quad_perm:[2,3,0,1] row_mask:0xf bank_mask:0xf
	v_pk_add_f32 v[10:11], v[10:11], v[26:27]
	v_pk_add_f32 v[12:13], v[12:13], v[28:29]
	v_max_f32_dpp v41, v41, v41 row_half_mirror row_mask:0xf bank_mask:0xf
	v_pk_add_f32 v[14:15], v[14:15], v[30:31]
	v_pk_add_f32 v[16:17], v[16:17], v[32:33]
	v_max_f32_dpp v41, v41, v41 row_mirror row_mask:0xf bank_mask:0xf
	s_nop 1
	v_max_f32_dpp v41, v41, v41 row_bcast:15 row_mask:0xa bank_mask:0xf
	s_nop 1
	v_max_f32_dpp v41, v41, v41 row_bcast:31 row_mask:0xc bank_mask:0xf
	s_nop 1
	v_readlane_b32 s28, v41, 63
	s_nop 1
	v_div_scale_f32 v48, s[30:31], s28, s28, v47
	v_rcp_f32_e32 v49, v48
	s_nop 0
	v_fma_f32 v50, -v48, v49, 1.0
	v_fmac_f32_e32 v49, v50, v49
	v_mov_b32_e32 v50, s28
	v_div_scale_f32 v50, vcc, s32, v50, s32
	v_mul_f32_e32 v51, v50, v49
	v_fma_f32 v52, -v48, v51, v50
	v_fmac_f32_e32 v51, v52, v49
	v_fma_f32 v48, -v48, v51, v50
	v_div_fmas_f32 v48, v48, v49, v51
	v_div_fixup_f32 v48, v48, s28, v47
	v_cmp_gt_f32_e64 vcc, s28, 0
	v_writelane_b32 v40, s28, 0
	s_nop 0
	v_cndmask_b32_e32 v48, 0, v48, vcc
	v_fmaak_f32 v49, v18, v48, 0x4b400000
	v_fmaak_f32 v50, v19, v48, 0x4b400000
	v_fmaak_f32 v51, v20, v48, 0x4b400000
	v_fmaak_f32 v52, v21, v48, 0x4b400000
	v_perm_b32 v49, v50, v49, s33
	v_perm_b32 v51, v52, v51, s34
	v_or_b32_e32 v56, v49, v51
	v_fmaak_f32 v41, v22, v48, 0x4b400000
	v_fmaak_f32 v42, v23, v48, 0x4b400000
	v_fmaak_f32 v43, v24, v48, 0x4b400000
	v_fmaak_f32 v44, v25, v48, 0x4b400000
	v_perm_b32 v41, v42, v41, s33
	v_perm_b32 v43, v44, v43, s34
	v_or_b32_e32 v57, v41, v43
	v_fmaak_f32 v49, v26, v48, 0x4b400000
	v_fmaak_f32 v50, v27, v48, 0x4b400000
	v_fmaak_f32 v51, v28, v48, 0x4b400000
	v_fmaak_f32 v52, v29, v48, 0x4b400000
	v_perm_b32 v49, v50, v49, s33
	v_perm_b32 v51, v52, v51, s34
	v_or_b32_e32 v58, v49, v51
	v_fmaak_f32 v41, v30, v48, 0x4b400000
	v_fmaak_f32 v42, v31, v48, 0x4b400000
	v_fmaak_f32 v43, v32, v48, 0x4b400000
	v_fmaak_f32 v44, v33, v48, 0x4b400000
	v_perm_b32 v41, v42, v41, s33
	v_perm_b32 v43, v44, v43, s34
	v_or_b32_e32 v59, v41, v43
	s_waitcnt vmcnt(0)
	ds_read_b128 v[18:21], v38 offset:4096
	ds_read_b128 v[22:25], v38 offset:5120
	ds_read_b128 v[26:29], v38 offset:6144
	ds_read_b128 v[30:33], v38 offset:7168
	s_waitcnt lgkmcnt(0)
	s_mov_b32 m0, s35
	s_nop 0
	global_load_lds_dwordx4 v34, s[16:17] sc1 nt
	global_load_lds_dwordx4 v34, s[16:17] offset:1024 sc1 nt
	global_load_lds_dwordx4 v34, s[16:17] offset:2048 sc1 nt
	global_load_lds_dwordx4 v35, s[16:17] offset:3072 sc1 nt
	s_add_u32 s16, s16, 0x7d00
	s_addc_u32 s17, s17, 0
	v_cndmask_b32_e64 v30, 0, v30, s[18:19]
	v_cndmask_b32_e64 v31, 0, v31, s[18:19]
	v_cndmask_b32_e64 v32, 0, v32, s[18:19]
	v_cndmask_b32_e64 v33, 0, v33, s[18:19]
	v_max3_f32 v41, |v18|, |v19|, |v20|
	v_max3_f32 v42, |v21|, |v22|, |v23|
	v_max3_f32 v43, |v24|, |v25|, |v26|
	v_max3_f32 v44, |v27|, |v28|, |v29|
	v_max3_f32 v48, |v30|, |v31|, |v32|
	v_max3_f32 v41, v41, v42, |v33|
	v_max3_f32 v43, v43, v44, v48
	v_max_f32_e32 v41, v41, v43
	v_pk_add_f32 v[2:3], v[2:3], v[18:19]
	v_pk_add_f32 v[4:5], v[4:5], v[20:21]
	v_max_f32_dpp v41, v41, v41 quad_perm:[1,0,3,2] row_mask:0xf bank_mask:0xf
	v_pk_add_f32 v[6:7], v[6:7], v[22:23]
	v_pk_add_f32 v[8:9], v[8:9], v[24:25]
	v_max_f32_dpp v41, v41, v41 quad_perm:[2,3,0,1] row_mask:0xf bank_mask:0xf
	v_pk_add_f32 v[10:11], v[10:11], v[26:27]
	v_pk_add_f32 v[12:13], v[12:13], v[28:29]
	v_max_f32_dpp v41, v41, v41 row_half_mirror row_mask:0xf bank_mask:0xf
	v_pk_add_f32 v[14:15], v[14:15], v[30:31]
	v_pk_add_f32 v[16:17], v[16:17], v[32:33]
	v_max_f32_dpp v41, v41, v41 row_mirror row_mask:0xf bank_mask:0xf
	s_nop 1
	v_max_f32_dpp v41, v41, v41 row_bcast:15 row_mask:0xa bank_mask:0xf
	s_nop 1
	v_max_f32_dpp v41, v41, v41 row_bcast:31 row_mask:0xc bank_mask:0xf
	s_nop 1
	v_readlane_b32 s28, v41, 63
	s_nop 1
	v_div_scale_f32 v48, s[30:31], s28, s28, v47
	v_rcp_f32_e32 v49, v48
	s_nop 0
	v_fma_f32 v50, -v48, v49, 1.0
	v_fmac_f32_e32 v49, v50, v49
	v_mov_b32_e32 v50, s28
	v_div_scale_f32 v50, vcc, s32, v50, s32
	v_mul_f32_e32 v51, v50, v49
	v_fma_f32 v52, -v48, v51, v50
	v_fmac_f32_e32 v51, v52, v49
	v_fma_f32 v48, -v48, v51, v50
	v_div_fmas_f32 v48, v48, v49, v51
	v_div_fixup_f32 v48, v48, s28, v47
	v_cmp_gt_f32_e64 vcc, s28, 0
	v_writelane_b32 v40, s28, 1
	s_nop 0
	v_cndmask_b32_e32 v48, 0, v48, vcc
	v_fmaak_f32 v49, v18, v48, 0x4b400000
	v_fmaak_f32 v50, v19, v48, 0x4b400000
	v_fmaak_f32 v51, v20, v48, 0x4b400000
	v_fmaak_f32 v52, v21, v48, 0x4b400000
	v_perm_b32 v49, v50, v49, s33
	v_perm_b32 v51, v52, v51, s34
	v_or_b32_e32 v60, v49, v51
	v_fmaak_f32 v41, v22, v48, 0x4b400000
	v_fmaak_f32 v42, v23, v48, 0x4b400000
	v_fmaak_f32 v43, v24, v48, 0x4b400000
	v_fmaak_f32 v44, v25, v48, 0x4b400000
	v_perm_b32 v41, v42, v41, s33
	v_perm_b32 v43, v44, v43, s34
	v_or_b32_e32 v61, v41, v43
	v_fmaak_f32 v49, v26, v48, 0x4b400000
	v_fmaak_f32 v50, v27, v48, 0x4b400000
	v_fmaak_f32 v51, v28, v48, 0x4b400000
	v_fmaak_f32 v52, v29, v48, 0x4b400000
	v_perm_b32 v49, v50, v49, s33
	v_perm_b32 v51, v52, v51, s34
	v_or_b32_e32 v62, v49, v51
	v_fmaak_f32 v41, v30, v48, 0x4b400000
	v_fmaak_f32 v42, v31, v48, 0x4b400000
	v_fmaak_f32 v43, v32, v48, 0x4b400000
	v_fmaak_f32 v44, v33, v48, 0x4b400000
	v_perm_b32 v41, v42, v41, s33
	v_perm_b32 v43, v44, v43, s34
	v_or_b32_e32 v63, v41, v43
	s_waitcnt vmcnt(0)
	ds_read_b128 v[18:21], v38 offset:0
	ds_read_b128 v[22:25], v38 offset:1024
	ds_read_b128 v[26:29], v38 offset:2048
	ds_read_b128 v[30:33], v38 offset:3072
	s_waitcnt lgkmcnt(0)
	s_mov_b32 m0, s36
	s_nop 0
	global_load_lds_dwordx4 v34, s[16:17] sc1 nt
	global_load_lds_dwordx4 v34, s[16:17] offset:1024 sc1 nt
	global_load_lds_dwordx4 v34, s[16:17] offset:2048 sc1 nt
	global_load_lds_dwordx4 v35, s[16:17] offset:3072 sc1 nt
	s_add_u32 s16, s16, 0x7d00
	s_addc_u32 s17, s17, 0
	v_cndmask_b32_e64 v30, 0, v30, s[18:19]
	v_cndmask_b32_e64 v31, 0, v31, s[18:19]
	v_cndmask_b32_e64 v32, 0, v32, s[18:19]
	v_cndmask_b32_e64 v33, 0, v33, s[18:19]
	v_max3_f32 v41, |v18|, |v19|, |v20|
	v_max3_f32 v42, |v21|, |v22|, |v23|
	v_max3_f32 v43, |v24|, |v25|, |v26|
	v_max3_f32 v44, |v27|, |v28|, |v29|
	v_max3_f32 v48, |v30|, |v31|, |v32|
	v_max3_f32 v41, v41, v42, |v33|
	v_max3_f32 v43, v43, v44, v48
	v_max_f32_e32 v41, v41, v43
	v_pk_add_f32 v[2:3], v[2:3], v[18:19]
	v_pk_add_f32 v[4:5], v[4:5], v[20:21]
	v_max_f32_dpp v41, v41, v41 quad_perm:[1,0,3,2] row_mask:0xf bank_mask:0xf
	v_pk_add_f32 v[6:7], v[6:7], v[22:23]
	v_pk_add_f32 v[8:9], v[8:9], v[24:25]
	v_max_f32_dpp v41, v41, v41 quad_perm:[2,3,0,1] row_mask:0xf bank_mask:0xf
	v_pk_add_f32 v[10:11], v[10:11], v[26:27]
	v_pk_add_f32 v[12:13], v[12:13], v[28:29]
	v_max_f32_dpp v41, v41, v41 row_half_mirror row_mask:0xf bank_mask:0xf
	v_pk_add_f32 v[14:15], v[14:15], v[30:31]
	v_pk_add_f32 v[16:17], v[16:17], v[32:33]
	v_max_f32_dpp v41, v41, v41 row_mirror row_mask:0xf bank_mask:0xf
	s_nop 1
	v_max_f32_dpp v41, v41, v41 row_bcast:15 row_mask:0xa bank_mask:0xf
	s_nop 1
	v_max_f32_dpp v41, v41, v41 row_bcast:31 row_mask:0xc bank_mask:0xf
	s_nop 1
	v_readlane_b32 s28, v41, 63
	s_nop 1
	v_div_scale_f32 v48, s[30:31], s28, s28, v47
	v_rcp_f32_e32 v49, v48
	s_nop 0
	v_fma_f32 v50, -v48, v49, 1.0
	v_fmac_f32_e32 v49, v50, v49
	v_mov_b32_e32 v50, s28
	v_div_scale_f32 v50, vcc, s32, v50, s32
	v_mul_f32_e32 v51, v50, v49
	v_fma_f32 v52, -v48, v51, v50
	v_fmac_f32_e32 v51, v52, v49
	v_fma_f32 v48, -v48, v51, v50
	v_div_fmas_f32 v48, v48, v49, v51
	v_div_fixup_f32 v48, v48, s28, v47
	v_cmp_gt_f32_e64 vcc, s28, 0
	v_writelane_b32 v40, s28, 2
	s_nop 0
	v_cndmask_b32_e32 v48, 0, v48, vcc
	v_fmaak_f32 v49, v18, v48, 0x4b400000
	v_fmaak_f32 v50, v19, v48, 0x4b400000
	v_fmaak_f32 v51, v20, v48, 0x4b400000
	v_fmaak_f32 v52, v21, v48, 0x4b400000
	v_perm_b32 v49, v50, v49, s33
	v_perm_b32 v51, v52, v51, s34
	v_or_b32_e32 v64, v49, v51
	v_fmaak_f32 v41, v22, v48, 0x4b400000
	v_fmaak_f32 v42, v23, v48, 0x4b400000
	v_fmaak_f32 v43, v24, v48, 0x4b400000
	v_fmaak_f32 v44, v25, v48, 0x4b400000
	v_perm_b32 v41, v42, v41, s33
	v_perm_b32 v43, v44, v43, s34
	v_or_b32_e32 v65, v41, v43
	v_fmaak_f32 v49, v26, v48, 0x4b400000
	v_fmaak_f32 v50, v27, v48, 0x4b400000
	v_fmaak_f32 v51, v28, v48, 0x4b400000
	v_fmaak_f32 v52, v29, v48, 0x4b400000
	v_perm_b32 v49, v50, v49, s33
	v_perm_b32 v51, v52, v51, s34
	v_or_b32_e32 v66, v49, v51
	v_fmaak_f32 v41, v30, v48, 0x4b400000
	v_fmaak_f32 v42, v31, v48, 0x4b400000
	v_fmaak_f32 v43, v32, v48, 0x4b400000
	v_fmaak_f32 v44, v33, v48, 0x4b400000
	v_perm_b32 v41, v42, v41, s33
	v_perm_b32 v43, v44, v43, s34
	v_or_b32_e32 v67, v41, v43
	s_waitcnt vmcnt(0)
	ds_read_b128 v[18:21], v38 offset:4096
	ds_read_b128 v[22:25], v38 offset:5120
	ds_read_b128 v[26:29], v38 offset:6144
	ds_read_b128 v[30:33], v38 offset:7168
	s_waitcnt lgkmcnt(0)
	s_mov_b32 m0, s35
	s_nop 0
	global_load_lds_dwordx4 v34, s[16:17] sc1 nt
	global_load_lds_dwordx4 v34, s[16:17] offset:1024 sc1 nt
	global_load_lds_dwordx4 v34, s[16:17] offset:2048 sc1 nt
	global_load_lds_dwordx4 v35, s[16:17] offset:3072 sc1 nt
	s_add_u32 s16, s16, 0x7d00
	s_addc_u32 s17, s17, 0
	v_cndmask_b32_e64 v30, 0, v30, s[18:19]
	v_cndmask_b32_e64 v31, 0, v31, s[18:19]
	v_cndmask_b32_e64 v32, 0, v32, s[18:19]
	v_cndmask_b32_e64 v33, 0, v33, s[18:19]
	v_max3_f32 v41, |v18|, |v19|, |v20|
	v_max3_f32 v42, |v21|, |v22|, |v23|
	v_max3_f32 v43, |v24|, |v25|, |v26|
	v_max3_f32 v44, |v27|, |v28|, |v29|
	v_max3_f32 v48, |v30|, |v31|, |v32|
	v_max3_f32 v41, v41, v42, |v33|
	v_max3_f32 v43, v43, v44, v48
	v_max_f32_e32 v41, v41, v43
	v_pk_add_f32 v[2:3], v[2:3], v[18:19]
	v_pk_add_f32 v[4:5], v[4:5], v[20:21]
	v_max_f32_dpp v41, v41, v41 quad_perm:[1,0,3,2] row_mask:0xf bank_mask:0xf
	v_pk_add_f32 v[6:7], v[6:7], v[22:23]
	v_pk_add_f32 v[8:9], v[8:9], v[24:25]
	v_max_f32_dpp v41, v41, v41 quad_perm:[2,3,0,1] row_mask:0xf bank_mask:0xf
	v_pk_add_f32 v[10:11], v[10:11], v[26:27]
	v_pk_add_f32 v[12:13], v[12:13], v[28:29]
	v_max_f32_dpp v41, v41, v41 row_half_mirror row_mask:0xf bank_mask:0xf
	v_pk_add_f32 v[14:15], v[14:15], v[30:31]
	v_pk_add_f32 v[16:17], v[16:17], v[32:33]
	v_max_f32_dpp v41, v41, v41 row_mirror row_mask:0xf bank_mask:0xf
	s_nop 1
	v_max_f32_dpp v41, v41, v41 row_bcast:15 row_mask:0xa bank_mask:0xf
	s_nop 1
	v_max_f32_dpp v41, v41, v41 row_bcast:31 row_mask:0xc bank_mask:0xf
	s_nop 1
	v_readlane_b32 s28, v41, 63
	s_nop 1
	v_div_scale_f32 v48, s[30:31], s28, s28, v47
	v_rcp_f32_e32 v49, v48
	s_nop 0
	v_fma_f32 v50, -v48, v49, 1.0
	v_fmac_f32_e32 v49, v50, v49
	v_mov_b32_e32 v50, s28
	v_div_scale_f32 v50, vcc, s32, v50, s32
	v_mul_f32_e32 v51, v50, v49
	v_fma_f32 v52, -v48, v51, v50
	v_fmac_f32_e32 v51, v52, v49
	v_fma_f32 v48, -v48, v51, v50
	v_div_fmas_f32 v48, v48, v49, v51
	v_div_fixup_f32 v48, v48, s28, v47
	v_cmp_gt_f32_e64 vcc, s28, 0
	v_writelane_b32 v40, s28, 3
	s_nop 0
	v_cndmask_b32_e32 v48, 0, v48, vcc
	v_fmaak_f32 v49, v18, v48, 0x4b400000
	v_fmaak_f32 v50, v19, v48, 0x4b400000
	v_fmaak_f32 v51, v20, v48, 0x4b400000
	v_fmaak_f32 v52, v21, v48, 0x4b400000
	v_perm_b32 v49, v50, v49, s33
	v_perm_b32 v51, v52, v51, s34
	v_or_b32_e32 v68, v49, v51
	v_fmaak_f32 v41, v22, v48, 0x4b400000
	v_fmaak_f32 v42, v23, v48, 0x4b400000
	v_fmaak_f32 v43, v24, v48, 0x4b400000
	v_fmaak_f32 v44, v25, v48, 0x4b400000
	v_perm_b32 v41, v42, v41, s33
	v_perm_b32 v43, v44, v43, s34
	v_or_b32_e32 v69, v41, v43
	v_fmaak_f32 v49, v26, v48, 0x4b400000
	v_fmaak_f32 v50, v27, v48, 0x4b400000
	v_fmaak_f32 v51, v28, v48, 0x4b400000
	v_fmaak_f32 v52, v29, v48, 0x4b400000
	v_perm_b32 v49, v50, v49, s33
	v_perm_b32 v51, v52, v51, s34
	v_or_b32_e32 v70, v49, v51
	v_fmaak_f32 v41, v30, v48, 0x4b400000
	v_fmaak_f32 v42, v31, v48, 0x4b400000
	v_fmaak_f32 v43, v32, v48, 0x4b400000
	v_fmaak_f32 v44, v33, v48, 0x4b400000
	v_perm_b32 v41, v42, v41, s33
	v_perm_b32 v43, v44, v43, s34
	v_or_b32_e32 v71, v41, v43
	s_waitcnt vmcnt(0)
	ds_read_b128 v[18:21], v38 offset:0
	ds_read_b128 v[22:25], v38 offset:1024
	ds_read_b128 v[26:29], v38 offset:2048
	ds_read_b128 v[30:33], v38 offset:3072
	s_waitcnt lgkmcnt(0)
	s_mov_b32 m0, s36
	s_nop 0
	global_load_lds_dwordx4 v34, s[16:17] sc1 nt
	global_load_lds_dwordx4 v34, s[16:17] offset:1024 sc1 nt
	global_load_lds_dwordx4 v34, s[16:17] offset:2048 sc1 nt
	global_load_lds_dwordx4 v35, s[16:17] offset:3072 sc1 nt
	s_add_u32 s16, s16, 0x7d00
	s_addc_u32 s17, s17, 0
	v_cndmask_b32_e64 v30, 0, v30, s[18:19]
	v_cndmask_b32_e64 v31, 0, v31, s[18:19]
	v_cndmask_b32_e64 v32, 0, v32, s[18:19]
	v_cndmask_b32_e64 v33, 0, v33, s[18:19]
	v_max3_f32 v41, |v18|, |v19|, |v20|
	v_max3_f32 v42, |v21|, |v22|, |v23|
	v_max3_f32 v43, |v24|, |v25|, |v26|
	v_max3_f32 v44, |v27|, |v28|, |v29|
	v_max3_f32 v48, |v30|, |v31|, |v32|
	v_max3_f32 v41, v41, v42, |v33|
	v_max3_f32 v43, v43, v44, v48
	v_max_f32_e32 v41, v41, v43
	v_pk_add_f32 v[2:3], v[2:3], v[18:19]
	v_pk_add_f32 v[4:5], v[4:5], v[20:21]
	v_max_f32_dpp v41, v41, v41 quad_perm:[1,0,3,2] row_mask:0xf bank_mask:0xf
	v_pk_add_f32 v[6:7], v[6:7], v[22:23]
	v_pk_add_f32 v[8:9], v[8:9], v[24:25]
	v_max_f32_dpp v41, v41, v41 quad_perm:[2,3,0,1] row_mask:0xf bank_mask:0xf
	v_pk_add_f32 v[10:11], v[10:11], v[26:27]
	v_pk_add_f32 v[12:13], v[12:13], v[28:29]
	v_max_f32_dpp v41, v41, v41 row_half_mirror row_mask:0xf bank_mask:0xf
	v_pk_add_f32 v[14:15], v[14:15], v[30:31]
	v_pk_add_f32 v[16:17], v[16:17], v[32:33]
	v_max_f32_dpp v41, v41, v41 row_mirror row_mask:0xf bank_mask:0xf
	s_nop 1
	v_max_f32_dpp v41, v41, v41 row_bcast:15 row_mask:0xa bank_mask:0xf
	s_nop 1
	v_max_f32_dpp v41, v41, v41 row_bcast:31 row_mask:0xc bank_mask:0xf
	s_nop 1
	v_readlane_b32 s28, v41, 63
	s_nop 1
	v_div_scale_f32 v48, s[30:31], s28, s28, v47
	v_rcp_f32_e32 v49, v48
	s_nop 0
	v_fma_f32 v50, -v48, v49, 1.0
	v_fmac_f32_e32 v49, v50, v49
	v_mov_b32_e32 v50, s28
	v_div_scale_f32 v50, vcc, s32, v50, s32
	v_mul_f32_e32 v51, v50, v49
	v_fma_f32 v52, -v48, v51, v50
	v_fmac_f32_e32 v51, v52, v49
	v_fma_f32 v48, -v48, v51, v50
	v_div_fmas_f32 v48, v48, v49, v51
	v_div_fixup_f32 v48, v48, s28, v47
	v_cmp_gt_f32_e64 vcc, s28, 0
	v_writelane_b32 v40, s28, 4
	s_nop 0
	v_cndmask_b32_e32 v48, 0, v48, vcc
	v_fmaak_f32 v49, v18, v48, 0x4b400000
	v_fmaak_f32 v50, v19, v48, 0x4b400000
	v_fmaak_f32 v51, v20, v48, 0x4b400000
	v_fmaak_f32 v52, v21, v48, 0x4b400000
	v_perm_b32 v49, v50, v49, s33
	v_perm_b32 v51, v52, v51, s34
	v_or_b32_e32 v72, v49, v51
	v_fmaak_f32 v41, v22, v48, 0x4b400000
	v_fmaak_f32 v42, v23, v48, 0x4b400000
	v_fmaak_f32 v43, v24, v48, 0x4b400000
	v_fmaak_f32 v44, v25, v48, 0x4b400000
	v_perm_b32 v41, v42, v41, s33
	v_perm_b32 v43, v44, v43, s34
	v_or_b32_e32 v73, v41, v43
	v_fmaak_f32 v49, v26, v48, 0x4b400000
	v_fmaak_f32 v50, v27, v48, 0x4b400000
	v_fmaak_f32 v51, v28, v48, 0x4b400000
	v_fmaak_f32 v52, v29, v48, 0x4b400000
	v_perm_b32 v49, v50, v49, s33
	v_perm_b32 v51, v52, v51, s34
	v_or_b32_e32 v74, v49, v51
	v_fmaak_f32 v41, v30, v48, 0x4b400000
	v_fmaak_f32 v42, v31, v48, 0x4b400000
	v_fmaak_f32 v43, v32, v48, 0x4b400000
	v_fmaak_f32 v44, v33, v48, 0x4b400000
	v_perm_b32 v41, v42, v41, s33
	v_perm_b32 v43, v44, v43, s34
	v_or_b32_e32 v75, v41, v43
	s_waitcnt vmcnt(0)
	ds_read_b128 v[18:21], v38 offset:4096
	ds_read_b128 v[22:25], v38 offset:5120
	ds_read_b128 v[26:29], v38 offset:6144
	ds_read_b128 v[30:33], v38 offset:7168
	s_waitcnt lgkmcnt(0)
	s_mov_b32 m0, s35
	s_nop 0
	global_load_lds_dwordx4 v34, s[16:17] sc1 nt
	global_load_lds_dwordx4 v34, s[16:17] offset:1024 sc1 nt
	global_load_lds_dwordx4 v34, s[16:17] offset:2048 sc1 nt
	global_load_lds_dwordx4 v35, s[16:17] offset:3072 sc1 nt
	s_add_u32 s16, s16, 0x7d00
	s_addc_u32 s17, s17, 0
	v_cndmask_b32_e64 v30, 0, v30, s[18:19]
	v_cndmask_b32_e64 v31, 0, v31, s[18:19]
	v_cndmask_b32_e64 v32, 0, v32, s[18:19]
	v_cndmask_b32_e64 v33, 0, v33, s[18:19]
	v_max3_f32 v41, |v18|, |v19|, |v20|
	v_max3_f32 v42, |v21|, |v22|, |v23|
	v_max3_f32 v43, |v24|, |v25|, |v26|
	v_max3_f32 v44, |v27|, |v28|, |v29|
	v_max3_f32 v48, |v30|, |v31|, |v32|
	v_max3_f32 v41, v41, v42, |v33|
	v_max3_f32 v43, v43, v44, v48
	v_max_f32_e32 v41, v41, v43
	v_pk_add_f32 v[2:3], v[2:3], v[18:19]
	v_pk_add_f32 v[4:5], v[4:5], v[20:21]
	v_max_f32_dpp v41, v41, v41 quad_perm:[1,0,3,2] row_mask:0xf bank_mask:0xf
	v_pk_add_f32 v[6:7], v[6:7], v[22:23]
	v_pk_add_f32 v[8:9], v[8:9], v[24:25]
	v_max_f32_dpp v41, v41, v41 quad_perm:[2,3,0,1] row_mask:0xf bank_mask:0xf
	v_pk_add_f32 v[10:11], v[10:11], v[26:27]
	v_pk_add_f32 v[12:13], v[12:13], v[28:29]
	v_max_f32_dpp v41, v41, v41 row_half_mirror row_mask:0xf bank_mask:0xf
	v_pk_add_f32 v[14:15], v[14:15], v[30:31]
	v_pk_add_f32 v[16:17], v[16:17], v[32:33]
	v_max_f32_dpp v41, v41, v41 row_mirror row_mask:0xf bank_mask:0xf
	s_nop 1
	v_max_f32_dpp v41, v41, v41 row_bcast:15 row_mask:0xa bank_mask:0xf
	s_nop 1
	v_max_f32_dpp v41, v41, v41 row_bcast:31 row_mask:0xc bank_mask:0xf
	s_nop 1
	v_readlane_b32 s28, v41, 63
	s_nop 1
	v_div_scale_f32 v48, s[30:31], s28, s28, v47
	v_rcp_f32_e32 v49, v48
	s_nop 0
	v_fma_f32 v50, -v48, v49, 1.0
	v_fmac_f32_e32 v49, v50, v49
	v_mov_b32_e32 v50, s28
	v_div_scale_f32 v50, vcc, s32, v50, s32
	v_mul_f32_e32 v51, v50, v49
	v_fma_f32 v52, -v48, v51, v50
	v_fmac_f32_e32 v51, v52, v49
	v_fma_f32 v48, -v48, v51, v50
	v_div_fmas_f32 v48, v48, v49, v51
	v_div_fixup_f32 v48, v48, s28, v47
	v_cmp_gt_f32_e64 vcc, s28, 0
	v_writelane_b32 v40, s28, 5
	s_nop 0
	v_cndmask_b32_e32 v48, 0, v48, vcc
	v_fmaak_f32 v49, v18, v48, 0x4b400000
	v_fmaak_f32 v50, v19, v48, 0x4b400000
	v_fmaak_f32 v51, v20, v48, 0x4b400000
	v_fmaak_f32 v52, v21, v48, 0x4b400000
	v_perm_b32 v49, v50, v49, s33
	v_perm_b32 v51, v52, v51, s34
	v_or_b32_e32 v76, v49, v51
	v_fmaak_f32 v41, v22, v48, 0x4b400000
	v_fmaak_f32 v42, v23, v48, 0x4b400000
	v_fmaak_f32 v43, v24, v48, 0x4b400000
	v_fmaak_f32 v44, v25, v48, 0x4b400000
	v_perm_b32 v41, v42, v41, s33
	v_perm_b32 v43, v44, v43, s34
	v_or_b32_e32 v77, v41, v43
	v_fmaak_f32 v49, v26, v48, 0x4b400000
	v_fmaak_f32 v50, v27, v48, 0x4b400000
	v_fmaak_f32 v51, v28, v48, 0x4b400000
	v_fmaak_f32 v52, v29, v48, 0x4b400000
	v_perm_b32 v49, v50, v49, s33
	v_perm_b32 v51, v52, v51, s34
	v_or_b32_e32 v78, v49, v51
	v_fmaak_f32 v41, v30, v48, 0x4b400000
	v_fmaak_f32 v42, v31, v48, 0x4b400000
	v_fmaak_f32 v43, v32, v48, 0x4b400000
	v_fmaak_f32 v44, v33, v48, 0x4b400000
	v_perm_b32 v41, v42, v41, s33
	v_perm_b32 v43, v44, v43, s34
	v_or_b32_e32 v79, v41, v43
	s_waitcnt vmcnt(0)
	ds_read_b128 v[18:21], v38 offset:0
	ds_read_b128 v[22:25], v38 offset:1024
	ds_read_b128 v[26:29], v38 offset:2048
	ds_read_b128 v[30:33], v38 offset:3072
	s_waitcnt lgkmcnt(0)
	s_mov_b32 m0, s36
	s_nop 0
	global_load_lds_dwordx4 v34, s[16:17] sc1 nt
	global_load_lds_dwordx4 v34, s[16:17] offset:1024 sc1 nt
	global_load_lds_dwordx4 v34, s[16:17] offset:2048 sc1 nt
	global_load_lds_dwordx4 v35, s[16:17] offset:3072 sc1 nt
	s_add_u32 s16, s16, 0x7d00
	s_addc_u32 s17, s17, 0
	v_cndmask_b32_e64 v30, 0, v30, s[18:19]
	v_cndmask_b32_e64 v31, 0, v31, s[18:19]
	v_cndmask_b32_e64 v32, 0, v32, s[18:19]
	v_cndmask_b32_e64 v33, 0, v33, s[18:19]
	v_max3_f32 v41, |v18|, |v19|, |v20|
	v_max3_f32 v42, |v21|, |v22|, |v23|
	v_max3_f32 v43, |v24|, |v25|, |v26|
	v_max3_f32 v44, |v27|, |v28|, |v29|
	v_max3_f32 v48, |v30|, |v31|, |v32|
	v_max3_f32 v41, v41, v42, |v33|
	v_max3_f32 v43, v43, v44, v48
	v_max_f32_e32 v41, v41, v43
	v_pk_add_f32 v[2:3], v[2:3], v[18:19]
	v_pk_add_f32 v[4:5], v[4:5], v[20:21]
	v_max_f32_dpp v41, v41, v41 quad_perm:[1,0,3,2] row_mask:0xf bank_mask:0xf
	v_pk_add_f32 v[6:7], v[6:7], v[22:23]
	v_pk_add_f32 v[8:9], v[8:9], v[24:25]
	v_max_f32_dpp v41, v41, v41 quad_perm:[2,3,0,1] row_mask:0xf bank_mask:0xf
	v_pk_add_f32 v[10:11], v[10:11], v[26:27]
	v_pk_add_f32 v[12:13], v[12:13], v[28:29]
	v_max_f32_dpp v41, v41, v41 row_half_mirror row_mask:0xf bank_mask:0xf
	v_pk_add_f32 v[14:15], v[14:15], v[30:31]
	v_pk_add_f32 v[16:17], v[16:17], v[32:33]
	v_max_f32_dpp v41, v41, v41 row_mirror row_mask:0xf bank_mask:0xf
	s_nop 1
	v_max_f32_dpp v41, v41, v41 row_bcast:15 row_mask:0xa bank_mask:0xf
	s_nop 1
	v_max_f32_dpp v41, v41, v41 row_bcast:31 row_mask:0xc bank_mask:0xf
	s_nop 1
	v_readlane_b32 s28, v41, 63
	s_nop 1
	v_div_scale_f32 v48, s[30:31], s28, s28, v47
	v_rcp_f32_e32 v49, v48
	s_nop 0
	v_fma_f32 v50, -v48, v49, 1.0
	v_fmac_f32_e32 v49, v50, v49
	v_mov_b32_e32 v50, s28
	v_div_scale_f32 v50, vcc, s32, v50, s32
	v_mul_f32_e32 v51, v50, v49
	v_fma_f32 v52, -v48, v51, v50
	v_fmac_f32_e32 v51, v52, v49
	v_fma_f32 v48, -v48, v51, v50
	v_div_fmas_f32 v48, v48, v49, v51
	v_div_fixup_f32 v48, v48, s28, v47
	v_cmp_gt_f32_e64 vcc, s28, 0
	v_writelane_b32 v40, s28, 6
	s_nop 0
	v_cndmask_b32_e32 v48, 0, v48, vcc
	v_fmaak_f32 v49, v18, v48, 0x4b400000
	v_fmaak_f32 v50, v19, v48, 0x4b400000
	v_fmaak_f32 v51, v20, v48, 0x4b400000
	v_fmaak_f32 v52, v21, v48, 0x4b400000
	v_perm_b32 v49, v50, v49, s33
	v_perm_b32 v51, v52, v51, s34
	v_or_b32_e32 v80, v49, v51
	v_fmaak_f32 v41, v22, v48, 0x4b400000
	v_fmaak_f32 v42, v23, v48, 0x4b400000
	v_fmaak_f32 v43, v24, v48, 0x4b400000
	v_fmaak_f32 v44, v25, v48, 0x4b400000
	v_perm_b32 v41, v42, v41, s33
	v_perm_b32 v43, v44, v43, s34
	v_or_b32_e32 v81, v41, v43
	v_fmaak_f32 v49, v26, v48, 0x4b400000
	v_fmaak_f32 v50, v27, v48, 0x4b400000
	v_fmaak_f32 v51, v28, v48, 0x4b400000
	v_fmaak_f32 v52, v29, v48, 0x4b400000
	v_perm_b32 v49, v50, v49, s33
	v_perm_b32 v51, v52, v51, s34
	v_or_b32_e32 v82, v49, v51
	v_fmaak_f32 v41, v30, v48, 0x4b400000
	v_fmaak_f32 v42, v31, v48, 0x4b400000
	v_fmaak_f32 v43, v32, v48, 0x4b400000
	v_fmaak_f32 v44, v33, v48, 0x4b400000
	v_perm_b32 v41, v42, v41, s33
	v_perm_b32 v43, v44, v43, s34
	v_or_b32_e32 v83, v41, v43
	s_waitcnt vmcnt(0)
	ds_read_b128 v[18:21], v38 offset:4096
	ds_read_b128 v[22:25], v38 offset:5120
	ds_read_b128 v[26:29], v38 offset:6144
	ds_read_b128 v[30:33], v38 offset:7168
	s_waitcnt lgkmcnt(0)
	s_mov_b32 m0, s35
	s_nop 0
	global_load_lds_dwordx4 v34, s[16:17] sc1 nt
	global_load_lds_dwordx4 v34, s[16:17] offset:1024 sc1 nt
	global_load_lds_dwordx4 v34, s[16:17] offset:2048 sc1 nt
	global_load_lds_dwordx4 v35, s[16:17] offset:3072 sc1 nt
	s_add_u32 s16, s16, 0x7d00
	s_addc_u32 s17, s17, 0
	v_cndmask_b32_e64 v30, 0, v30, s[18:19]
	v_cndmask_b32_e64 v31, 0, v31, s[18:19]
	v_cndmask_b32_e64 v32, 0, v32, s[18:19]
	v_cndmask_b32_e64 v33, 0, v33, s[18:19]
	v_max3_f32 v41, |v18|, |v19|, |v20|
	v_max3_f32 v42, |v21|, |v22|, |v23|
	v_max3_f32 v43, |v24|, |v25|, |v26|
	v_max3_f32 v44, |v27|, |v28|, |v29|
	v_max3_f32 v48, |v30|, |v31|, |v32|
	v_max3_f32 v41, v41, v42, |v33|
	v_max3_f32 v43, v43, v44, v48
	v_max_f32_e32 v41, v41, v43
	v_pk_add_f32 v[2:3], v[2:3], v[18:19]
	v_pk_add_f32 v[4:5], v[4:5], v[20:21]
	v_max_f32_dpp v41, v41, v41 quad_perm:[1,0,3,2] row_mask:0xf bank_mask:0xf
	v_pk_add_f32 v[6:7], v[6:7], v[22:23]
	v_pk_add_f32 v[8:9], v[8:9], v[24:25]
	v_max_f32_dpp v41, v41, v41 quad_perm:[2,3,0,1] row_mask:0xf bank_mask:0xf
	v_pk_add_f32 v[10:11], v[10:11], v[26:27]
	v_pk_add_f32 v[12:13], v[12:13], v[28:29]
	v_max_f32_dpp v41, v41, v41 row_half_mirror row_mask:0xf bank_mask:0xf
	v_pk_add_f32 v[14:15], v[14:15], v[30:31]
	v_pk_add_f32 v[16:17], v[16:17], v[32:33]
	v_max_f32_dpp v41, v41, v41 row_mirror row_mask:0xf bank_mask:0xf
	s_nop 1
	v_max_f32_dpp v41, v41, v41 row_bcast:15 row_mask:0xa bank_mask:0xf
	s_nop 1
	v_max_f32_dpp v41, v41, v41 row_bcast:31 row_mask:0xc bank_mask:0xf
	s_nop 1
	v_readlane_b32 s28, v41, 63
	s_nop 1
	v_div_scale_f32 v48, s[30:31], s28, s28, v47
	v_rcp_f32_e32 v49, v48
	s_nop 0
	v_fma_f32 v50, -v48, v49, 1.0
	v_fmac_f32_e32 v49, v50, v49
	v_mov_b32_e32 v50, s28
	v_div_scale_f32 v50, vcc, s32, v50, s32
	v_mul_f32_e32 v51, v50, v49
	v_fma_f32 v52, -v48, v51, v50
	v_fmac_f32_e32 v51, v52, v49
	v_fma_f32 v48, -v48, v51, v50
	v_div_fmas_f32 v48, v48, v49, v51
	v_div_fixup_f32 v48, v48, s28, v47
	v_cmp_gt_f32_e64 vcc, s28, 0
	v_writelane_b32 v40, s28, 7
	s_nop 0
	v_cndmask_b32_e32 v48, 0, v48, vcc
	v_fmaak_f32 v49, v18, v48, 0x4b400000
	v_fmaak_f32 v50, v19, v48, 0x4b400000
	v_fmaak_f32 v51, v20, v48, 0x4b400000
	v_fmaak_f32 v52, v21, v48, 0x4b400000
	v_perm_b32 v49, v50, v49, s33
	v_perm_b32 v51, v52, v51, s34
	v_or_b32_e32 v84, v49, v51
	v_fmaak_f32 v41, v22, v48, 0x4b400000
	v_fmaak_f32 v42, v23, v48, 0x4b400000
	v_fmaak_f32 v43, v24, v48, 0x4b400000
	v_fmaak_f32 v44, v25, v48, 0x4b400000
	v_perm_b32 v41, v42, v41, s33
	v_perm_b32 v43, v44, v43, s34
	v_or_b32_e32 v85, v41, v43
	v_fmaak_f32 v49, v26, v48, 0x4b400000
	v_fmaak_f32 v50, v27, v48, 0x4b400000
	v_fmaak_f32 v51, v28, v48, 0x4b400000
	v_fmaak_f32 v52, v29, v48, 0x4b400000
	v_perm_b32 v49, v50, v49, s33
	v_perm_b32 v51, v52, v51, s34
	v_or_b32_e32 v86, v49, v51
	v_fmaak_f32 v41, v30, v48, 0x4b400000
	v_fmaak_f32 v42, v31, v48, 0x4b400000
	v_fmaak_f32 v43, v32, v48, 0x4b400000
	v_fmaak_f32 v44, v33, v48, 0x4b400000
	v_perm_b32 v41, v42, v41, s33
	v_perm_b32 v43, v44, v43, s34
	v_or_b32_e32 v87, v41, v43
	s_waitcnt vmcnt(0)
	ds_read_b128 v[18:21], v38 offset:0
	ds_read_b128 v[22:25], v38 offset:1024
	ds_read_b128 v[26:29], v38 offset:2048
	ds_read_b128 v[30:33], v38 offset:3072
	s_waitcnt lgkmcnt(0)
	s_mov_b32 m0, s36
	s_nop 0
	global_load_lds_dwordx4 v34, s[16:17] sc1 nt
	global_load_lds_dwordx4 v34, s[16:17] offset:1024 sc1 nt
	global_load_lds_dwordx4 v34, s[16:17] offset:2048 sc1 nt
	global_load_lds_dwordx4 v35, s[16:17] offset:3072 sc1 nt
	s_add_u32 s16, s16, 0x7d00
	s_addc_u32 s17, s17, 0
	v_cndmask_b32_e64 v30, 0, v30, s[18:19]
	v_cndmask_b32_e64 v31, 0, v31, s[18:19]
	v_cndmask_b32_e64 v32, 0, v32, s[18:19]
	v_cndmask_b32_e64 v33, 0, v33, s[18:19]
	v_max3_f32 v41, |v18|, |v19|, |v20|
	v_max3_f32 v42, |v21|, |v22|, |v23|
	v_max3_f32 v43, |v24|, |v25|, |v26|
	v_max3_f32 v44, |v27|, |v28|, |v29|
	v_max3_f32 v48, |v30|, |v31|, |v32|
	v_max3_f32 v41, v41, v42, |v33|
	v_max3_f32 v43, v43, v44, v48
	v_max_f32_e32 v41, v41, v43
	v_pk_add_f32 v[2:3], v[2:3], v[18:19]
	v_pk_add_f32 v[4:5], v[4:5], v[20:21]
	v_max_f32_dpp v41, v41, v41 quad_perm:[1,0,3,2] row_mask:0xf bank_mask:0xf
	v_pk_add_f32 v[6:7], v[6:7], v[22:23]
	v_pk_add_f32 v[8:9], v[8:9], v[24:25]
	v_max_f32_dpp v41, v41, v41 quad_perm:[2,3,0,1] row_mask:0xf bank_mask:0xf
	v_pk_add_f32 v[10:11], v[10:11], v[26:27]
	v_pk_add_f32 v[12:13], v[12:13], v[28:29]
	v_max_f32_dpp v41, v41, v41 row_half_mirror row_mask:0xf bank_mask:0xf
	v_pk_add_f32 v[14:15], v[14:15], v[30:31]
	v_pk_add_f32 v[16:17], v[16:17], v[32:33]
	v_max_f32_dpp v41, v41, v41 row_mirror row_mask:0xf bank_mask:0xf
	s_nop 1
	v_max_f32_dpp v41, v41, v41 row_bcast:15 row_mask:0xa bank_mask:0xf
	s_nop 1
	v_max_f32_dpp v41, v41, v41 row_bcast:31 row_mask:0xc bank_mask:0xf
	s_nop 1
	v_readlane_b32 s28, v41, 63
	s_nop 1
	v_div_scale_f32 v48, s[30:31], s28, s28, v47
	v_rcp_f32_e32 v49, v48
	s_nop 0
	v_fma_f32 v50, -v48, v49, 1.0
	v_fmac_f32_e32 v49, v50, v49
	v_mov_b32_e32 v50, s28
	v_div_scale_f32 v50, vcc, s32, v50, s32
	v_mul_f32_e32 v51, v50, v49
	v_fma_f32 v52, -v48, v51, v50
	v_fmac_f32_e32 v51, v52, v49
	v_fma_f32 v48, -v48, v51, v50
	v_div_fmas_f32 v48, v48, v49, v51
	v_div_fixup_f32 v48, v48, s28, v47
	v_cmp_gt_f32_e64 vcc, s28, 0
	v_writelane_b32 v40, s28, 8
	s_nop 0
	v_cndmask_b32_e32 v48, 0, v48, vcc
	v_fmaak_f32 v49, v18, v48, 0x4b400000
	v_fmaak_f32 v50, v19, v48, 0x4b400000
	v_fmaak_f32 v51, v20, v48, 0x4b400000
	v_fmaak_f32 v52, v21, v48, 0x4b400000
	v_perm_b32 v49, v50, v49, s33
	v_perm_b32 v51, v52, v51, s34
	v_or_b32_e32 v88, v49, v51
	v_fmaak_f32 v41, v22, v48, 0x4b400000
	v_fmaak_f32 v42, v23, v48, 0x4b400000
	v_fmaak_f32 v43, v24, v48, 0x4b400000
	v_fmaak_f32 v44, v25, v48, 0x4b400000
	v_perm_b32 v41, v42, v41, s33
	v_perm_b32 v43, v44, v43, s34
	v_or_b32_e32 v89, v41, v43
	v_fmaak_f32 v49, v26, v48, 0x4b400000
	v_fmaak_f32 v50, v27, v48, 0x4b400000
	v_fmaak_f32 v51, v28, v48, 0x4b400000
	v_fmaak_f32 v52, v29, v48, 0x4b400000
	v_perm_b32 v49, v50, v49, s33
	v_perm_b32 v51, v52, v51, s34
	v_or_b32_e32 v90, v49, v51
	v_fmaak_f32 v41, v30, v48, 0x4b400000
	v_fmaak_f32 v42, v31, v48, 0x4b400000
	v_fmaak_f32 v43, v32, v48, 0x4b400000
	v_fmaak_f32 v44, v33, v48, 0x4b400000
	v_perm_b32 v41, v42, v41, s33
	v_perm_b32 v43, v44, v43, s34
	v_or_b32_e32 v91, v41, v43
	s_waitcnt vmcnt(0)
	ds_read_b128 v[18:21], v38 offset:4096
	ds_read_b128 v[22:25], v38 offset:5120
	ds_read_b128 v[26:29], v38 offset:6144
	ds_read_b128 v[30:33], v38 offset:7168
	s_waitcnt lgkmcnt(0)
	s_mov_b32 m0, s35
	s_nop 0
	global_load_lds_dwordx4 v34, s[16:17] sc1 nt
	global_load_lds_dwordx4 v34, s[16:17] offset:1024 sc1 nt
	global_load_lds_dwordx4 v34, s[16:17] offset:2048 sc1 nt
	global_load_lds_dwordx4 v35, s[16:17] offset:3072 sc1 nt
	s_add_u32 s16, s16, 0x7d00
	s_addc_u32 s17, s17, 0
	v_cndmask_b32_e64 v30, 0, v30, s[18:19]
	v_cndmask_b32_e64 v31, 0, v31, s[18:19]
	v_cndmask_b32_e64 v32, 0, v32, s[18:19]
	v_cndmask_b32_e64 v33, 0, v33, s[18:19]
	v_max3_f32 v41, |v18|, |v19|, |v20|
	v_max3_f32 v42, |v21|, |v22|, |v23|
	v_max3_f32 v43, |v24|, |v25|, |v26|
	v_max3_f32 v44, |v27|, |v28|, |v29|
	v_max3_f32 v48, |v30|, |v31|, |v32|
	v_max3_f32 v41, v41, v42, |v33|
	v_max3_f32 v43, v43, v44, v48
	v_max_f32_e32 v41, v41, v43
	v_pk_add_f32 v[2:3], v[2:3], v[18:19]
	v_pk_add_f32 v[4:5], v[4:5], v[20:21]
	v_max_f32_dpp v41, v41, v41 quad_perm:[1,0,3,2] row_mask:0xf bank_mask:0xf
	v_pk_add_f32 v[6:7], v[6:7], v[22:23]
	v_pk_add_f32 v[8:9], v[8:9], v[24:25]
	v_max_f32_dpp v41, v41, v41 quad_perm:[2,3,0,1] row_mask:0xf bank_mask:0xf
	v_pk_add_f32 v[10:11], v[10:11], v[26:27]
	v_pk_add_f32 v[12:13], v[12:13], v[28:29]
	v_max_f32_dpp v41, v41, v41 row_half_mirror row_mask:0xf bank_mask:0xf
	v_pk_add_f32 v[14:15], v[14:15], v[30:31]
	v_pk_add_f32 v[16:17], v[16:17], v[32:33]
	v_max_f32_dpp v41, v41, v41 row_mirror row_mask:0xf bank_mask:0xf
	s_nop 1
	v_max_f32_dpp v41, v41, v41 row_bcast:15 row_mask:0xa bank_mask:0xf
	s_nop 1
	v_max_f32_dpp v41, v41, v41 row_bcast:31 row_mask:0xc bank_mask:0xf
	s_nop 1
	v_readlane_b32 s28, v41, 63
	s_nop 1
	v_div_scale_f32 v48, s[30:31], s28, s28, v47
	v_rcp_f32_e32 v49, v48
	s_nop 0
	v_fma_f32 v50, -v48, v49, 1.0
	v_fmac_f32_e32 v49, v50, v49
	v_mov_b32_e32 v50, s28
	v_div_scale_f32 v50, vcc, s32, v50, s32
	v_mul_f32_e32 v51, v50, v49
	v_fma_f32 v52, -v48, v51, v50
	v_fmac_f32_e32 v51, v52, v49
	v_fma_f32 v48, -v48, v51, v50
	v_div_fmas_f32 v48, v48, v49, v51
	v_div_fixup_f32 v48, v48, s28, v47
	v_cmp_gt_f32_e64 vcc, s28, 0
	v_writelane_b32 v40, s28, 9
	s_nop 0
	v_cndmask_b32_e32 v48, 0, v48, vcc
	v_fmaak_f32 v49, v18, v48, 0x4b400000
	v_fmaak_f32 v50, v19, v48, 0x4b400000
	v_fmaak_f32 v51, v20, v48, 0x4b400000
	v_fmaak_f32 v52, v21, v48, 0x4b400000
	v_perm_b32 v49, v50, v49, s33
	v_perm_b32 v51, v52, v51, s34
	v_or_b32_e32 v92, v49, v51
	v_fmaak_f32 v41, v22, v48, 0x4b400000
	v_fmaak_f32 v42, v23, v48, 0x4b400000
	v_fmaak_f32 v43, v24, v48, 0x4b400000
	v_fmaak_f32 v44, v25, v48, 0x4b400000
	v_perm_b32 v41, v42, v41, s33
	v_perm_b32 v43, v44, v43, s34
	v_or_b32_e32 v93, v41, v43
	v_fmaak_f32 v49, v26, v48, 0x4b400000
	v_fmaak_f32 v50, v27, v48, 0x4b400000
	v_fmaak_f32 v51, v28, v48, 0x4b400000
	v_fmaak_f32 v52, v29, v48, 0x4b400000
	v_perm_b32 v49, v50, v49, s33
	v_perm_b32 v51, v52, v51, s34
	v_or_b32_e32 v94, v49, v51
	v_fmaak_f32 v41, v30, v48, 0x4b400000
	v_fmaak_f32 v42, v31, v48, 0x4b400000
	v_fmaak_f32 v43, v32, v48, 0x4b400000
	v_fmaak_f32 v44, v33, v48, 0x4b400000
	v_perm_b32 v41, v42, v41, s33
	v_perm_b32 v43, v44, v43, s34
	v_or_b32_e32 v95, v41, v43
	s_waitcnt vmcnt(0)
	ds_read_b128 v[18:21], v38 offset:0
	ds_read_b128 v[22:25], v38 offset:1024
	ds_read_b128 v[26:29], v38 offset:2048
	ds_read_b128 v[30:33], v38 offset:3072
	s_waitcnt lgkmcnt(0)
	s_mov_b32 m0, s36
	s_nop 0
	global_load_lds_dwordx4 v34, s[16:17] sc1 nt
	global_load_lds_dwordx4 v34, s[16:17] offset:1024 sc1 nt
	global_load_lds_dwordx4 v34, s[16:17] offset:2048 sc1 nt
	global_load_lds_dwordx4 v35, s[16:17] offset:3072 sc1 nt
	s_add_u32 s16, s16, 0x7d00
	s_addc_u32 s17, s17, 0
	v_cndmask_b32_e64 v30, 0, v30, s[18:19]
	v_cndmask_b32_e64 v31, 0, v31, s[18:19]
	v_cndmask_b32_e64 v32, 0, v32, s[18:19]
	v_cndmask_b32_e64 v33, 0, v33, s[18:19]
	v_max3_f32 v41, |v18|, |v19|, |v20|
	v_max3_f32 v42, |v21|, |v22|, |v23|
	v_max3_f32 v43, |v24|, |v25|, |v26|
	v_max3_f32 v44, |v27|, |v28|, |v29|
	v_max3_f32 v48, |v30|, |v31|, |v32|
	v_max3_f32 v41, v41, v42, |v33|
	v_max3_f32 v43, v43, v44, v48
	v_max_f32_e32 v41, v41, v43
	v_pk_add_f32 v[2:3], v[2:3], v[18:19]
	v_pk_add_f32 v[4:5], v[4:5], v[20:21]
	v_max_f32_dpp v41, v41, v41 quad_perm:[1,0,3,2] row_mask:0xf bank_mask:0xf
	v_pk_add_f32 v[6:7], v[6:7], v[22:23]
	v_pk_add_f32 v[8:9], v[8:9], v[24:25]
	v_max_f32_dpp v41, v41, v41 quad_perm:[2,3,0,1] row_mask:0xf bank_mask:0xf
	v_pk_add_f32 v[10:11], v[10:11], v[26:27]
	v_pk_add_f32 v[12:13], v[12:13], v[28:29]
	v_max_f32_dpp v41, v41, v41 row_half_mirror row_mask:0xf bank_mask:0xf
	v_pk_add_f32 v[14:15], v[14:15], v[30:31]
	v_pk_add_f32 v[16:17], v[16:17], v[32:33]
	v_max_f32_dpp v41, v41, v41 row_mirror row_mask:0xf bank_mask:0xf
	s_nop 1
	v_max_f32_dpp v41, v41, v41 row_bcast:15 row_mask:0xa bank_mask:0xf
	s_nop 1
	v_max_f32_dpp v41, v41, v41 row_bcast:31 row_mask:0xc bank_mask:0xf
	s_nop 1
	v_readlane_b32 s28, v41, 63
	s_nop 1
	v_div_scale_f32 v48, s[30:31], s28, s28, v47
	v_rcp_f32_e32 v49, v48
	s_nop 0
	v_fma_f32 v50, -v48, v49, 1.0
	v_fmac_f32_e32 v49, v50, v49
	v_mov_b32_e32 v50, s28
	v_div_scale_f32 v50, vcc, s32, v50, s32
	v_mul_f32_e32 v51, v50, v49
	v_fma_f32 v52, -v48, v51, v50
	v_fmac_f32_e32 v51, v52, v49
	v_fma_f32 v48, -v48, v51, v50
	v_div_fmas_f32 v48, v48, v49, v51
	v_div_fixup_f32 v48, v48, s28, v47
	v_cmp_gt_f32_e64 vcc, s28, 0
	v_writelane_b32 v40, s28, 10
	s_nop 0
	v_cndmask_b32_e32 v48, 0, v48, vcc
	v_fmaak_f32 v49, v18, v48, 0x4b400000
	v_fmaak_f32 v50, v19, v48, 0x4b400000
	v_fmaak_f32 v51, v20, v48, 0x4b400000
	v_fmaak_f32 v52, v21, v48, 0x4b400000
	v_perm_b32 v49, v50, v49, s33
	v_perm_b32 v51, v52, v51, s34
	v_or_b32_e32 v96, v49, v51
	v_fmaak_f32 v41, v22, v48, 0x4b400000
	v_fmaak_f32 v42, v23, v48, 0x4b400000
	v_fmaak_f32 v43, v24, v48, 0x4b400000
	v_fmaak_f32 v44, v25, v48, 0x4b400000
	v_perm_b32 v41, v42, v41, s33
	v_perm_b32 v43, v44, v43, s34
	v_or_b32_e32 v97, v41, v43
	v_fmaak_f32 v49, v26, v48, 0x4b400000
	v_fmaak_f32 v50, v27, v48, 0x4b400000
	v_fmaak_f32 v51, v28, v48, 0x4b400000
	v_fmaak_f32 v52, v29, v48, 0x4b400000
	v_perm_b32 v49, v50, v49, s33
	v_perm_b32 v51, v52, v51, s34
	v_or_b32_e32 v98, v49, v51
	v_fmaak_f32 v41, v30, v48, 0x4b400000
	v_fmaak_f32 v42, v31, v48, 0x4b400000
	v_fmaak_f32 v43, v32, v48, 0x4b400000
	v_fmaak_f32 v44, v33, v48, 0x4b400000
	v_perm_b32 v41, v42, v41, s33
	v_perm_b32 v43, v44, v43, s34
	v_or_b32_e32 v99, v41, v43
	s_waitcnt vmcnt(0)
	ds_read_b128 v[18:21], v38 offset:4096
	ds_read_b128 v[22:25], v38 offset:5120
	ds_read_b128 v[26:29], v38 offset:6144
	ds_read_b128 v[30:33], v38 offset:7168
	s_waitcnt lgkmcnt(0)
	s_mov_b32 m0, s35
	s_nop 0
	global_load_lds_dwordx4 v34, s[16:17] sc1 nt
	global_load_lds_dwordx4 v34, s[16:17] offset:1024 sc1 nt
	global_load_lds_dwordx4 v34, s[16:17] offset:2048 sc1 nt
	global_load_lds_dwordx4 v35, s[16:17] offset:3072 sc1 nt
	s_add_u32 s16, s16, 0x7d00
	s_addc_u32 s17, s17, 0
	v_cndmask_b32_e64 v30, 0, v30, s[18:19]
	v_cndmask_b32_e64 v31, 0, v31, s[18:19]
	v_cndmask_b32_e64 v32, 0, v32, s[18:19]
	v_cndmask_b32_e64 v33, 0, v33, s[18:19]
	v_max3_f32 v41, |v18|, |v19|, |v20|
	v_max3_f32 v42, |v21|, |v22|, |v23|
	v_max3_f32 v43, |v24|, |v25|, |v26|
	v_max3_f32 v44, |v27|, |v28|, |v29|
	v_max3_f32 v48, |v30|, |v31|, |v32|
	v_max3_f32 v41, v41, v42, |v33|
	v_max3_f32 v43, v43, v44, v48
	v_max_f32_e32 v41, v41, v43
	v_pk_add_f32 v[2:3], v[2:3], v[18:19]
	v_pk_add_f32 v[4:5], v[4:5], v[20:21]
	v_max_f32_dpp v41, v41, v41 quad_perm:[1,0,3,2] row_mask:0xf bank_mask:0xf
	v_pk_add_f32 v[6:7], v[6:7], v[22:23]
	v_pk_add_f32 v[8:9], v[8:9], v[24:25]
	v_max_f32_dpp v41, v41, v41 quad_perm:[2,3,0,1] row_mask:0xf bank_mask:0xf
	v_pk_add_f32 v[10:11], v[10:11], v[26:27]
	v_pk_add_f32 v[12:13], v[12:13], v[28:29]
	v_max_f32_dpp v41, v41, v41 row_half_mirror row_mask:0xf bank_mask:0xf
	v_pk_add_f32 v[14:15], v[14:15], v[30:31]
	v_pk_add_f32 v[16:17], v[16:17], v[32:33]
	v_max_f32_dpp v41, v41, v41 row_mirror row_mask:0xf bank_mask:0xf
	s_nop 1
	v_max_f32_dpp v41, v41, v41 row_bcast:15 row_mask:0xa bank_mask:0xf
	s_nop 1
	v_max_f32_dpp v41, v41, v41 row_bcast:31 row_mask:0xc bank_mask:0xf
	s_nop 1
	v_readlane_b32 s28, v41, 63
	s_nop 1
	v_div_scale_f32 v48, s[30:31], s28, s28, v47
	v_rcp_f32_e32 v49, v48
	s_nop 0
	v_fma_f32 v50, -v48, v49, 1.0
	v_fmac_f32_e32 v49, v50, v49
	v_mov_b32_e32 v50, s28
	v_div_scale_f32 v50, vcc, s32, v50, s32
	v_mul_f32_e32 v51, v50, v49
	v_fma_f32 v52, -v48, v51, v50
	v_fmac_f32_e32 v51, v52, v49
	v_fma_f32 v48, -v48, v51, v50
	v_div_fmas_f32 v48, v48, v49, v51
	v_div_fixup_f32 v48, v48, s28, v47
	v_cmp_gt_f32_e64 vcc, s28, 0
	v_writelane_b32 v40, s28, 11
	s_nop 0
	v_cndmask_b32_e32 v48, 0, v48, vcc
	v_fmaak_f32 v49, v18, v48, 0x4b400000
	v_fmaak_f32 v50, v19, v48, 0x4b400000
	v_fmaak_f32 v51, v20, v48, 0x4b400000
	v_fmaak_f32 v52, v21, v48, 0x4b400000
	v_perm_b32 v49, v50, v49, s33
	v_perm_b32 v51, v52, v51, s34
	v_or_b32_e32 v100, v49, v51
	v_fmaak_f32 v41, v22, v48, 0x4b400000
	v_fmaak_f32 v42, v23, v48, 0x4b400000
	v_fmaak_f32 v43, v24, v48, 0x4b400000
	v_fmaak_f32 v44, v25, v48, 0x4b400000
	v_perm_b32 v41, v42, v41, s33
	v_perm_b32 v43, v44, v43, s34
	v_or_b32_e32 v101, v41, v43
	v_fmaak_f32 v49, v26, v48, 0x4b400000
	v_fmaak_f32 v50, v27, v48, 0x4b400000
	v_fmaak_f32 v51, v28, v48, 0x4b400000
	v_fmaak_f32 v52, v29, v48, 0x4b400000
	v_perm_b32 v49, v50, v49, s33
	v_perm_b32 v51, v52, v51, s34
	v_or_b32_e32 v102, v49, v51
	v_fmaak_f32 v41, v30, v48, 0x4b400000
	v_fmaak_f32 v42, v31, v48, 0x4b400000
	v_fmaak_f32 v43, v32, v48, 0x4b400000
	v_fmaak_f32 v44, v33, v48, 0x4b400000
	v_perm_b32 v41, v42, v41, s33
	v_perm_b32 v43, v44, v43, s34
	v_or_b32_e32 v103, v41, v43
	s_waitcnt vmcnt(0)
	ds_read_b128 v[18:21], v38 offset:0
	ds_read_b128 v[22:25], v38 offset:1024
	ds_read_b128 v[26:29], v38 offset:2048
	ds_read_b128 v[30:33], v38 offset:3072
	s_waitcnt lgkmcnt(0)
	s_mov_b32 m0, s36
	s_nop 0
	global_load_lds_dwordx4 v34, s[16:17] sc1 nt
	global_load_lds_dwordx4 v34, s[16:17] offset:1024 sc1 nt
	global_load_lds_dwordx4 v34, s[16:17] offset:2048 sc1 nt
	global_load_lds_dwordx4 v35, s[16:17] offset:3072 sc1 nt
	s_add_u32 s16, s16, 0x7d00
	s_addc_u32 s17, s17, 0
	v_cndmask_b32_e64 v30, 0, v30, s[18:19]
	v_cndmask_b32_e64 v31, 0, v31, s[18:19]
	v_cndmask_b32_e64 v32, 0, v32, s[18:19]
	v_cndmask_b32_e64 v33, 0, v33, s[18:19]
	v_max3_f32 v41, |v18|, |v19|, |v20|
	v_max3_f32 v42, |v21|, |v22|, |v23|
	v_max3_f32 v43, |v24|, |v25|, |v26|
	v_max3_f32 v44, |v27|, |v28|, |v29|
	v_max3_f32 v48, |v30|, |v31|, |v32|
	v_max3_f32 v41, v41, v42, |v33|
	v_max3_f32 v43, v43, v44, v48
	v_max_f32_e32 v41, v41, v43
	v_pk_add_f32 v[2:3], v[2:3], v[18:19]
	v_pk_add_f32 v[4:5], v[4:5], v[20:21]
	v_max_f32_dpp v41, v41, v41 quad_perm:[1,0,3,2] row_mask:0xf bank_mask:0xf
	v_pk_add_f32 v[6:7], v[6:7], v[22:23]
	v_pk_add_f32 v[8:9], v[8:9], v[24:25]
	v_max_f32_dpp v41, v41, v41 quad_perm:[2,3,0,1] row_mask:0xf bank_mask:0xf
	v_pk_add_f32 v[10:11], v[10:11], v[26:27]
	v_pk_add_f32 v[12:13], v[12:13], v[28:29]
	v_max_f32_dpp v41, v41, v41 row_half_mirror row_mask:0xf bank_mask:0xf
	v_pk_add_f32 v[14:15], v[14:15], v[30:31]
	v_pk_add_f32 v[16:17], v[16:17], v[32:33]
	v_max_f32_dpp v41, v41, v41 row_mirror row_mask:0xf bank_mask:0xf
	s_nop 1
	v_max_f32_dpp v41, v41, v41 row_bcast:15 row_mask:0xa bank_mask:0xf
	s_nop 1
	v_max_f32_dpp v41, v41, v41 row_bcast:31 row_mask:0xc bank_mask:0xf
	s_nop 1
	v_readlane_b32 s28, v41, 63
	s_nop 1
	v_div_scale_f32 v48, s[30:31], s28, s28, v47
	v_rcp_f32_e32 v49, v48
	s_nop 0
	v_fma_f32 v50, -v48, v49, 1.0
	v_fmac_f32_e32 v49, v50, v49
	v_mov_b32_e32 v50, s28
	v_div_scale_f32 v50, vcc, s32, v50, s32
	v_mul_f32_e32 v51, v50, v49
	v_fma_f32 v52, -v48, v51, v50
	v_fmac_f32_e32 v51, v52, v49
	v_fma_f32 v48, -v48, v51, v50
	v_div_fmas_f32 v48, v48, v49, v51
	v_div_fixup_f32 v48, v48, s28, v47
	v_cmp_gt_f32_e64 vcc, s28, 0
	v_writelane_b32 v40, s28, 12
	s_nop 0
	v_cndmask_b32_e32 v48, 0, v48, vcc
	v_fmaak_f32 v49, v18, v48, 0x4b400000
	v_fmaak_f32 v50, v19, v48, 0x4b400000
	v_fmaak_f32 v51, v20, v48, 0x4b400000
	v_fmaak_f32 v52, v21, v48, 0x4b400000
	v_perm_b32 v49, v50, v49, s33
	v_perm_b32 v51, v52, v51, s34
	v_or_b32_e32 v104, v49, v51
	v_fmaak_f32 v41, v22, v48, 0x4b400000
	v_fmaak_f32 v42, v23, v48, 0x4b400000
	v_fmaak_f32 v43, v24, v48, 0x4b400000
	v_fmaak_f32 v44, v25, v48, 0x4b400000
	v_perm_b32 v41, v42, v41, s33
	v_perm_b32 v43, v44, v43, s34
	v_or_b32_e32 v105, v41, v43
	v_fmaak_f32 v49, v26, v48, 0x4b400000
	v_fmaak_f32 v50, v27, v48, 0x4b400000
	v_fmaak_f32 v51, v28, v48, 0x4b400000
	v_fmaak_f32 v52, v29, v48, 0x4b400000
	v_perm_b32 v49, v50, v49, s33
	v_perm_b32 v51, v52, v51, s34
	v_or_b32_e32 v106, v49, v51
	v_fmaak_f32 v41, v30, v48, 0x4b400000
	v_fmaak_f32 v42, v31, v48, 0x4b400000
	v_fmaak_f32 v43, v32, v48, 0x4b400000
	v_fmaak_f32 v44, v33, v48, 0x4b400000
	v_perm_b32 v41, v42, v41, s33
	v_perm_b32 v43, v44, v43, s34
	v_or_b32_e32 v107, v41, v43
	s_waitcnt vmcnt(0)
	ds_read_b128 v[18:21], v38 offset:4096
	ds_read_b128 v[22:25], v38 offset:5120
	ds_read_b128 v[26:29], v38 offset:6144
	ds_read_b128 v[30:33], v38 offset:7168
	s_waitcnt lgkmcnt(0)
	s_mov_b32 m0, s35
	s_nop 0
	global_load_lds_dwordx4 v34, s[16:17] sc1 nt
	global_load_lds_dwordx4 v34, s[16:17] offset:1024 sc1 nt
	global_load_lds_dwordx4 v34, s[16:17] offset:2048 sc1 nt
	global_load_lds_dwordx4 v35, s[16:17] offset:3072 sc1 nt
	s_add_u32 s16, s16, 0x7d00
	s_addc_u32 s17, s17, 0
	v_cndmask_b32_e64 v30, 0, v30, s[18:19]
	v_cndmask_b32_e64 v31, 0, v31, s[18:19]
	v_cndmask_b32_e64 v32, 0, v32, s[18:19]
	v_cndmask_b32_e64 v33, 0, v33, s[18:19]
	v_max3_f32 v41, |v18|, |v19|, |v20|
	v_max3_f32 v42, |v21|, |v22|, |v23|
	v_max3_f32 v43, |v24|, |v25|, |v26|
	v_max3_f32 v44, |v27|, |v28|, |v29|
	v_max3_f32 v48, |v30|, |v31|, |v32|
	v_max3_f32 v41, v41, v42, |v33|
	v_max3_f32 v43, v43, v44, v48
	v_max_f32_e32 v41, v41, v43
	v_pk_add_f32 v[2:3], v[2:3], v[18:19]
	v_pk_add_f32 v[4:5], v[4:5], v[20:21]
	v_max_f32_dpp v41, v41, v41 quad_perm:[1,0,3,2] row_mask:0xf bank_mask:0xf
	v_pk_add_f32 v[6:7], v[6:7], v[22:23]
	v_pk_add_f32 v[8:9], v[8:9], v[24:25]
	v_max_f32_dpp v41, v41, v41 quad_perm:[2,3,0,1] row_mask:0xf bank_mask:0xf
	v_pk_add_f32 v[10:11], v[10:11], v[26:27]
	v_pk_add_f32 v[12:13], v[12:13], v[28:29]
	v_max_f32_dpp v41, v41, v41 row_half_mirror row_mask:0xf bank_mask:0xf
	v_pk_add_f32 v[14:15], v[14:15], v[30:31]
	v_pk_add_f32 v[16:17], v[16:17], v[32:33]
	v_max_f32_dpp v41, v41, v41 row_mirror row_mask:0xf bank_mask:0xf
	s_nop 1
	v_max_f32_dpp v41, v41, v41 row_bcast:15 row_mask:0xa bank_mask:0xf
	s_nop 1
	v_max_f32_dpp v41, v41, v41 row_bcast:31 row_mask:0xc bank_mask:0xf
	s_nop 1
	v_readlane_b32 s28, v41, 63
	s_nop 1
	v_div_scale_f32 v48, s[30:31], s28, s28, v47
	v_rcp_f32_e32 v49, v48
	s_nop 0
	v_fma_f32 v50, -v48, v49, 1.0
	v_fmac_f32_e32 v49, v50, v49
	v_mov_b32_e32 v50, s28
	v_div_scale_f32 v50, vcc, s32, v50, s32
	v_mul_f32_e32 v51, v50, v49
	v_fma_f32 v52, -v48, v51, v50
	v_fmac_f32_e32 v51, v52, v49
	v_fma_f32 v48, -v48, v51, v50
	v_div_fmas_f32 v48, v48, v49, v51
	v_div_fixup_f32 v48, v48, s28, v47
	v_cmp_gt_f32_e64 vcc, s28, 0
	v_writelane_b32 v40, s28, 13
	s_nop 0
	v_cndmask_b32_e32 v48, 0, v48, vcc
	v_fmaak_f32 v49, v18, v48, 0x4b400000
	v_fmaak_f32 v50, v19, v48, 0x4b400000
	v_fmaak_f32 v51, v20, v48, 0x4b400000
	v_fmaak_f32 v52, v21, v48, 0x4b400000
	v_perm_b32 v49, v50, v49, s33
	v_perm_b32 v51, v52, v51, s34
	v_or_b32_e32 v108, v49, v51
	v_fmaak_f32 v41, v22, v48, 0x4b400000
	v_fmaak_f32 v42, v23, v48, 0x4b400000
	v_fmaak_f32 v43, v24, v48, 0x4b400000
	v_fmaak_f32 v44, v25, v48, 0x4b400000
	v_perm_b32 v41, v42, v41, s33
	v_perm_b32 v43, v44, v43, s34
	v_or_b32_e32 v109, v41, v43
	v_fmaak_f32 v49, v26, v48, 0x4b400000
	v_fmaak_f32 v50, v27, v48, 0x4b400000
	v_fmaak_f32 v51, v28, v48, 0x4b400000
	v_fmaak_f32 v52, v29, v48, 0x4b400000
	v_perm_b32 v49, v50, v49, s33
	v_perm_b32 v51, v52, v51, s34
	v_or_b32_e32 v110, v49, v51
	v_fmaak_f32 v41, v30, v48, 0x4b400000
	v_fmaak_f32 v42, v31, v48, 0x4b400000
	v_fmaak_f32 v43, v32, v48, 0x4b400000
	v_fmaak_f32 v44, v33, v48, 0x4b400000
	v_perm_b32 v41, v42, v41, s33
	v_perm_b32 v43, v44, v43, s34
	v_or_b32_e32 v111, v41, v43
	s_waitcnt vmcnt(0)
	ds_read_b128 v[18:21], v38 offset:0
	ds_read_b128 v[22:25], v38 offset:1024
	ds_read_b128 v[26:29], v38 offset:2048
	ds_read_b128 v[30:33], v38 offset:3072
	s_waitcnt lgkmcnt(0)
	s_mov_b32 m0, s36
	s_nop 0
	global_load_lds_dwordx4 v34, s[16:17] sc1 nt
	global_load_lds_dwordx4 v34, s[16:17] offset:1024 sc1 nt
	global_load_lds_dwordx4 v34, s[16:17] offset:2048 sc1 nt
	global_load_lds_dwordx4 v35, s[16:17] offset:3072 sc1 nt
	s_add_u32 s16, s16, 0x7d00
	s_addc_u32 s17, s17, 0
	v_cndmask_b32_e64 v30, 0, v30, s[18:19]
	v_cndmask_b32_e64 v31, 0, v31, s[18:19]
	v_cndmask_b32_e64 v32, 0, v32, s[18:19]
	v_cndmask_b32_e64 v33, 0, v33, s[18:19]
	v_max3_f32 v41, |v18|, |v19|, |v20|
	v_max3_f32 v42, |v21|, |v22|, |v23|
	v_max3_f32 v43, |v24|, |v25|, |v26|
	v_max3_f32 v44, |v27|, |v28|, |v29|
	v_max3_f32 v48, |v30|, |v31|, |v32|
	v_max3_f32 v41, v41, v42, |v33|
	v_max3_f32 v43, v43, v44, v48
	v_max_f32_e32 v41, v41, v43
	v_pk_add_f32 v[2:3], v[2:3], v[18:19]
	v_pk_add_f32 v[4:5], v[4:5], v[20:21]
	v_max_f32_dpp v41, v41, v41 quad_perm:[1,0,3,2] row_mask:0xf bank_mask:0xf
	v_pk_add_f32 v[6:7], v[6:7], v[22:23]
	v_pk_add_f32 v[8:9], v[8:9], v[24:25]
	v_max_f32_dpp v41, v41, v41 quad_perm:[2,3,0,1] row_mask:0xf bank_mask:0xf
	v_pk_add_f32 v[10:11], v[10:11], v[26:27]
	v_pk_add_f32 v[12:13], v[12:13], v[28:29]
	v_max_f32_dpp v41, v41, v41 row_half_mirror row_mask:0xf bank_mask:0xf
	v_pk_add_f32 v[14:15], v[14:15], v[30:31]
	v_pk_add_f32 v[16:17], v[16:17], v[32:33]
	v_max_f32_dpp v41, v41, v41 row_mirror row_mask:0xf bank_mask:0xf
	s_nop 1
	v_max_f32_dpp v41, v41, v41 row_bcast:15 row_mask:0xa bank_mask:0xf
	s_nop 1
	v_max_f32_dpp v41, v41, v41 row_bcast:31 row_mask:0xc bank_mask:0xf
	s_nop 1
	v_readlane_b32 s28, v41, 63
	s_nop 1
	v_div_scale_f32 v48, s[30:31], s28, s28, v47
	v_rcp_f32_e32 v49, v48
	s_nop 0
	v_fma_f32 v50, -v48, v49, 1.0
	v_fmac_f32_e32 v49, v50, v49
	v_mov_b32_e32 v50, s28
	v_div_scale_f32 v50, vcc, s32, v50, s32
	v_mul_f32_e32 v51, v50, v49
	v_fma_f32 v52, -v48, v51, v50
	v_fmac_f32_e32 v51, v52, v49
	v_fma_f32 v48, -v48, v51, v50
	v_div_fmas_f32 v48, v48, v49, v51
	v_div_fixup_f32 v48, v48, s28, v47
	v_cmp_gt_f32_e64 vcc, s28, 0
	v_writelane_b32 v40, s28, 14
	s_nop 0
	v_cndmask_b32_e32 v48, 0, v48, vcc
	v_fmaak_f32 v49, v18, v48, 0x4b400000
	v_fmaak_f32 v50, v19, v48, 0x4b400000
	v_fmaak_f32 v51, v20, v48, 0x4b400000
	v_fmaak_f32 v52, v21, v48, 0x4b400000
	v_perm_b32 v49, v50, v49, s33
	v_perm_b32 v51, v52, v51, s34
	v_or_b32_e32 v112, v49, v51
	v_fmaak_f32 v41, v22, v48, 0x4b400000
	v_fmaak_f32 v42, v23, v48, 0x4b400000
	v_fmaak_f32 v43, v24, v48, 0x4b400000
	v_fmaak_f32 v44, v25, v48, 0x4b400000
	v_perm_b32 v41, v42, v41, s33
	v_perm_b32 v43, v44, v43, s34
	v_or_b32_e32 v113, v41, v43
	v_fmaak_f32 v49, v26, v48, 0x4b400000
	v_fmaak_f32 v50, v27, v48, 0x4b400000
	v_fmaak_f32 v51, v28, v48, 0x4b400000
	v_fmaak_f32 v52, v29, v48, 0x4b400000
	v_perm_b32 v49, v50, v49, s33
	v_perm_b32 v51, v52, v51, s34
	v_or_b32_e32 v114, v49, v51
	v_fmaak_f32 v41, v30, v48, 0x4b400000
	v_fmaak_f32 v42, v31, v48, 0x4b400000
	v_fmaak_f32 v43, v32, v48, 0x4b400000
	v_fmaak_f32 v44, v33, v48, 0x4b400000
	v_perm_b32 v41, v42, v41, s33
	v_perm_b32 v43, v44, v43, s34
	v_or_b32_e32 v115, v41, v43
	s_waitcnt vmcnt(0)
	ds_read_b128 v[18:21], v38 offset:4096
	ds_read_b128 v[22:25], v38 offset:5120
	ds_read_b128 v[26:29], v38 offset:6144
	ds_read_b128 v[30:33], v38 offset:7168
	s_waitcnt lgkmcnt(0)
	s_mov_b32 m0, s35
	s_nop 0
	global_load_lds_dwordx4 v34, s[16:17] sc1 nt
	global_load_lds_dwordx4 v34, s[16:17] offset:1024 sc1 nt
	global_load_lds_dwordx4 v34, s[16:17] offset:2048 sc1 nt
	global_load_lds_dwordx4 v35, s[16:17] offset:3072 sc1 nt
	s_add_u32 s16, s16, 0x7d00
	s_addc_u32 s17, s17, 0
	v_cndmask_b32_e64 v30, 0, v30, s[18:19]
	v_cndmask_b32_e64 v31, 0, v31, s[18:19]
	v_cndmask_b32_e64 v32, 0, v32, s[18:19]
	v_cndmask_b32_e64 v33, 0, v33, s[18:19]
	v_max3_f32 v41, |v18|, |v19|, |v20|
	v_max3_f32 v42, |v21|, |v22|, |v23|
	v_max3_f32 v43, |v24|, |v25|, |v26|
	v_max3_f32 v44, |v27|, |v28|, |v29|
	v_max3_f32 v48, |v30|, |v31|, |v32|
	v_max3_f32 v41, v41, v42, |v33|
	v_max3_f32 v43, v43, v44, v48
	v_max_f32_e32 v41, v41, v43
	v_pk_add_f32 v[2:3], v[2:3], v[18:19]
	v_pk_add_f32 v[4:5], v[4:5], v[20:21]
	v_max_f32_dpp v41, v41, v41 quad_perm:[1,0,3,2] row_mask:0xf bank_mask:0xf
	v_pk_add_f32 v[6:7], v[6:7], v[22:23]
	v_pk_add_f32 v[8:9], v[8:9], v[24:25]
	v_max_f32_dpp v41, v41, v41 quad_perm:[2,3,0,1] row_mask:0xf bank_mask:0xf
	v_pk_add_f32 v[10:11], v[10:11], v[26:27]
	v_pk_add_f32 v[12:13], v[12:13], v[28:29]
	v_max_f32_dpp v41, v41, v41 row_half_mirror row_mask:0xf bank_mask:0xf
	v_pk_add_f32 v[14:15], v[14:15], v[30:31]
	v_pk_add_f32 v[16:17], v[16:17], v[32:33]
	v_max_f32_dpp v41, v41, v41 row_mirror row_mask:0xf bank_mask:0xf
	s_nop 1
	v_max_f32_dpp v41, v41, v41 row_bcast:15 row_mask:0xa bank_mask:0xf
	s_nop 1
	v_max_f32_dpp v41, v41, v41 row_bcast:31 row_mask:0xc bank_mask:0xf
	s_nop 1
	v_readlane_b32 s28, v41, 63
	s_nop 1
	v_div_scale_f32 v48, s[30:31], s28, s28, v47
	v_rcp_f32_e32 v49, v48
	s_nop 0
	v_fma_f32 v50, -v48, v49, 1.0
	v_fmac_f32_e32 v49, v50, v49
	v_mov_b32_e32 v50, s28
	v_div_scale_f32 v50, vcc, s32, v50, s32
	v_mul_f32_e32 v51, v50, v49
	v_fma_f32 v52, -v48, v51, v50
	v_fmac_f32_e32 v51, v52, v49
	v_fma_f32 v48, -v48, v51, v50
	v_div_fmas_f32 v48, v48, v49, v51
	v_div_fixup_f32 v48, v48, s28, v47
	v_cmp_gt_f32_e64 vcc, s28, 0
	v_writelane_b32 v40, s28, 15
	s_nop 0
	v_cndmask_b32_e32 v48, 0, v48, vcc
	v_fmaak_f32 v49, v18, v48, 0x4b400000
	v_fmaak_f32 v50, v19, v48, 0x4b400000
	v_fmaak_f32 v51, v20, v48, 0x4b400000
	v_fmaak_f32 v52, v21, v48, 0x4b400000
	v_perm_b32 v49, v50, v49, s33
	v_perm_b32 v51, v52, v51, s34
	v_or_b32_e32 v116, v49, v51
	v_fmaak_f32 v41, v22, v48, 0x4b400000
	v_fmaak_f32 v42, v23, v48, 0x4b400000
	v_fmaak_f32 v43, v24, v48, 0x4b400000
	v_fmaak_f32 v44, v25, v48, 0x4b400000
	v_perm_b32 v41, v42, v41, s33
	v_perm_b32 v43, v44, v43, s34
	v_or_b32_e32 v117, v41, v43
	v_fmaak_f32 v49, v26, v48, 0x4b400000
	v_fmaak_f32 v50, v27, v48, 0x4b400000
	v_fmaak_f32 v51, v28, v48, 0x4b400000
	v_fmaak_f32 v52, v29, v48, 0x4b400000
	v_perm_b32 v49, v50, v49, s33
	v_perm_b32 v51, v52, v51, s34
	v_or_b32_e32 v118, v49, v51
	v_fmaak_f32 v41, v30, v48, 0x4b400000
	v_fmaak_f32 v42, v31, v48, 0x4b400000
	v_fmaak_f32 v43, v32, v48, 0x4b400000
	v_fmaak_f32 v44, v33, v48, 0x4b400000
	v_perm_b32 v41, v42, v41, s33
	v_perm_b32 v43, v44, v43, s34
	v_or_b32_e32 v119, v41, v43
	s_waitcnt vmcnt(0)
	ds_read_b128 v[18:21], v38 offset:0
	ds_read_b128 v[22:25], v38 offset:1024
	ds_read_b128 v[26:29], v38 offset:2048
	ds_read_b128 v[30:33], v38 offset:3072
	s_waitcnt lgkmcnt(0)
	s_mov_b32 m0, s36
	s_nop 0
	global_load_lds_dwordx4 v34, s[16:17] sc1 nt
	global_load_lds_dwordx4 v34, s[16:17] offset:1024 sc1 nt
	global_load_lds_dwordx4 v34, s[16:17] offset:2048 sc1 nt
	global_load_lds_dwordx4 v35, s[16:17] offset:3072 sc1 nt
	s_add_u32 s16, s16, 0x7d00
	s_addc_u32 s17, s17, 0
	v_cndmask_b32_e64 v30, 0, v30, s[18:19]
	v_cndmask_b32_e64 v31, 0, v31, s[18:19]
	v_cndmask_b32_e64 v32, 0, v32, s[18:19]
	v_cndmask_b32_e64 v33, 0, v33, s[18:19]
	v_max3_f32 v41, |v18|, |v19|, |v20|
	v_max3_f32 v42, |v21|, |v22|, |v23|
	v_max3_f32 v43, |v24|, |v25|, |v26|
	v_max3_f32 v44, |v27|, |v28|, |v29|
	v_max3_f32 v48, |v30|, |v31|, |v32|
	v_max3_f32 v41, v41, v42, |v33|
	v_max3_f32 v43, v43, v44, v48
	v_max_f32_e32 v41, v41, v43
	v_pk_add_f32 v[2:3], v[2:3], v[18:19]
	v_pk_add_f32 v[4:5], v[4:5], v[20:21]
	v_max_f32_dpp v41, v41, v41 quad_perm:[1,0,3,2] row_mask:0xf bank_mask:0xf
	v_pk_add_f32 v[6:7], v[6:7], v[22:23]
	v_pk_add_f32 v[8:9], v[8:9], v[24:25]
	v_max_f32_dpp v41, v41, v41 quad_perm:[2,3,0,1] row_mask:0xf bank_mask:0xf
	v_pk_add_f32 v[10:11], v[10:11], v[26:27]
	v_pk_add_f32 v[12:13], v[12:13], v[28:29]
	v_max_f32_dpp v41, v41, v41 row_half_mirror row_mask:0xf bank_mask:0xf
	v_pk_add_f32 v[14:15], v[14:15], v[30:31]
	v_pk_add_f32 v[16:17], v[16:17], v[32:33]
	v_max_f32_dpp v41, v41, v41 row_mirror row_mask:0xf bank_mask:0xf
	s_nop 1
	v_max_f32_dpp v41, v41, v41 row_bcast:15 row_mask:0xa bank_mask:0xf
	s_nop 1
	v_max_f32_dpp v41, v41, v41 row_bcast:31 row_mask:0xc bank_mask:0xf
	s_nop 1
	v_readlane_b32 s28, v41, 63
	s_nop 1
	v_div_scale_f32 v48, s[30:31], s28, s28, v47
	v_rcp_f32_e32 v49, v48
	s_nop 0
	v_fma_f32 v50, -v48, v49, 1.0
	v_fmac_f32_e32 v49, v50, v49
	v_mov_b32_e32 v50, s28
	v_div_scale_f32 v50, vcc, s32, v50, s32
	v_mul_f32_e32 v51, v50, v49
	v_fma_f32 v52, -v48, v51, v50
	v_fmac_f32_e32 v51, v52, v49
	v_fma_f32 v48, -v48, v51, v50
	v_div_fmas_f32 v48, v48, v49, v51
	v_div_fixup_f32 v48, v48, s28, v47
	v_cmp_gt_f32_e64 vcc, s28, 0
	v_writelane_b32 v40, s28, 16
	s_nop 0
	v_cndmask_b32_e32 v48, 0, v48, vcc
	v_fmaak_f32 v49, v18, v48, 0x4b400000
	v_fmaak_f32 v50, v19, v48, 0x4b400000
	v_fmaak_f32 v51, v20, v48, 0x4b400000
	v_fmaak_f32 v52, v21, v48, 0x4b400000
	v_perm_b32 v49, v50, v49, s33
	v_perm_b32 v51, v52, v51, s34
	v_or_b32_e32 v120, v49, v51
	v_fmaak_f32 v41, v22, v48, 0x4b400000
	v_fmaak_f32 v42, v23, v48, 0x4b400000
	v_fmaak_f32 v43, v24, v48, 0x4b400000
	v_fmaak_f32 v44, v25, v48, 0x4b400000
	v_perm_b32 v41, v42, v41, s33
	v_perm_b32 v43, v44, v43, s34
	v_or_b32_e32 v121, v41, v43
	v_fmaak_f32 v49, v26, v48, 0x4b400000
	v_fmaak_f32 v50, v27, v48, 0x4b400000
	v_fmaak_f32 v51, v28, v48, 0x4b400000
	v_fmaak_f32 v52, v29, v48, 0x4b400000
	v_perm_b32 v49, v50, v49, s33
	v_perm_b32 v51, v52, v51, s34
	v_or_b32_e32 v122, v49, v51
	v_fmaak_f32 v41, v30, v48, 0x4b400000
	v_fmaak_f32 v42, v31, v48, 0x4b400000
	v_fmaak_f32 v43, v32, v48, 0x4b400000
	v_fmaak_f32 v44, v33, v48, 0x4b400000
	v_perm_b32 v41, v42, v41, s33
	v_perm_b32 v43, v44, v43, s34
	v_or_b32_e32 v123, v41, v43
	s_waitcnt vmcnt(0)
	ds_read_b128 v[18:21], v38 offset:4096
	ds_read_b128 v[22:25], v38 offset:5120
	ds_read_b128 v[26:29], v38 offset:6144
	ds_read_b128 v[30:33], v38 offset:7168
	s_waitcnt lgkmcnt(0)
	s_mov_b32 m0, s35
	s_nop 0
	global_load_lds_dwordx4 v34, s[16:17] sc1 nt
	global_load_lds_dwordx4 v34, s[16:17] offset:1024 sc1 nt
	global_load_lds_dwordx4 v34, s[16:17] offset:2048 sc1 nt
	global_load_lds_dwordx4 v35, s[16:17] offset:3072 sc1 nt
	s_add_u32 s16, s16, 0x7d00
	s_addc_u32 s17, s17, 0
	v_cndmask_b32_e64 v30, 0, v30, s[18:19]
	v_cndmask_b32_e64 v31, 0, v31, s[18:19]
	v_cndmask_b32_e64 v32, 0, v32, s[18:19]
	v_cndmask_b32_e64 v33, 0, v33, s[18:19]
	v_max3_f32 v41, |v18|, |v19|, |v20|
	v_max3_f32 v42, |v21|, |v22|, |v23|
	v_max3_f32 v43, |v24|, |v25|, |v26|
	v_max3_f32 v44, |v27|, |v28|, |v29|
	v_max3_f32 v48, |v30|, |v31|, |v32|
	v_max3_f32 v41, v41, v42, |v33|
	v_max3_f32 v43, v43, v44, v48
	v_max_f32_e32 v41, v41, v43
	v_pk_add_f32 v[2:3], v[2:3], v[18:19]
	v_pk_add_f32 v[4:5], v[4:5], v[20:21]
	v_max_f32_dpp v41, v41, v41 quad_perm:[1,0,3,2] row_mask:0xf bank_mask:0xf
	v_pk_add_f32 v[6:7], v[6:7], v[22:23]
	v_pk_add_f32 v[8:9], v[8:9], v[24:25]
	v_max_f32_dpp v41, v41, v41 quad_perm:[2,3,0,1] row_mask:0xf bank_mask:0xf
	v_pk_add_f32 v[10:11], v[10:11], v[26:27]
	v_pk_add_f32 v[12:13], v[12:13], v[28:29]
	v_max_f32_dpp v41, v41, v41 row_half_mirror row_mask:0xf bank_mask:0xf
	v_pk_add_f32 v[14:15], v[14:15], v[30:31]
	v_pk_add_f32 v[16:17], v[16:17], v[32:33]
	v_max_f32_dpp v41, v41, v41 row_mirror row_mask:0xf bank_mask:0xf
	s_nop 1
	v_max_f32_dpp v41, v41, v41 row_bcast:15 row_mask:0xa bank_mask:0xf
	s_nop 1
	v_max_f32_dpp v41, v41, v41 row_bcast:31 row_mask:0xc bank_mask:0xf
	s_nop 1
	v_readlane_b32 s28, v41, 63
	s_nop 1
	v_div_scale_f32 v48, s[30:31], s28, s28, v47
	v_rcp_f32_e32 v49, v48
	s_nop 0
	v_fma_f32 v50, -v48, v49, 1.0
	v_fmac_f32_e32 v49, v50, v49
	v_mov_b32_e32 v50, s28
	v_div_scale_f32 v50, vcc, s32, v50, s32
	v_mul_f32_e32 v51, v50, v49
	v_fma_f32 v52, -v48, v51, v50
	v_fmac_f32_e32 v51, v52, v49
	v_fma_f32 v48, -v48, v51, v50
	v_div_fmas_f32 v48, v48, v49, v51
	v_div_fixup_f32 v48, v48, s28, v47
	v_cmp_gt_f32_e64 vcc, s28, 0
	v_writelane_b32 v40, s28, 17
	s_nop 0
	v_cndmask_b32_e32 v48, 0, v48, vcc
	v_fmaak_f32 v49, v18, v48, 0x4b400000
	v_fmaak_f32 v50, v19, v48, 0x4b400000
	v_fmaak_f32 v51, v20, v48, 0x4b400000
	v_fmaak_f32 v52, v21, v48, 0x4b400000
	v_perm_b32 v49, v50, v49, s33
	v_perm_b32 v51, v52, v51, s34
	v_or_b32_e32 v124, v49, v51
	v_fmaak_f32 v41, v22, v48, 0x4b400000
	v_fmaak_f32 v42, v23, v48, 0x4b400000
	v_fmaak_f32 v43, v24, v48, 0x4b400000
	v_fmaak_f32 v44, v25, v48, 0x4b400000
	v_perm_b32 v41, v42, v41, s33
	v_perm_b32 v43, v44, v43, s34
	v_or_b32_e32 v125, v41, v43
	v_fmaak_f32 v49, v26, v48, 0x4b400000
	v_fmaak_f32 v50, v27, v48, 0x4b400000
	v_fmaak_f32 v51, v28, v48, 0x4b400000
	v_fmaak_f32 v52, v29, v48, 0x4b400000
	v_perm_b32 v49, v50, v49, s33
	v_perm_b32 v51, v52, v51, s34
	v_or_b32_e32 v126, v49, v51
	v_fmaak_f32 v41, v30, v48, 0x4b400000
	v_fmaak_f32 v42, v31, v48, 0x4b400000
	v_fmaak_f32 v43, v32, v48, 0x4b400000
	v_fmaak_f32 v44, v33, v48, 0x4b400000
	v_perm_b32 v41, v42, v41, s33
	v_perm_b32 v43, v44, v43, s34
	v_or_b32_e32 v127, v41, v43
	s_waitcnt vmcnt(0)
	ds_read_b128 v[18:21], v38 offset:0
	ds_read_b128 v[22:25], v38 offset:1024
	ds_read_b128 v[26:29], v38 offset:2048
	ds_read_b128 v[30:33], v38 offset:3072
	s_waitcnt lgkmcnt(0)
	s_mov_b32 m0, s36
	s_nop 0
	global_load_lds_dwordx4 v34, s[16:17] sc1 nt
	global_load_lds_dwordx4 v34, s[16:17] offset:1024 sc1 nt
	global_load_lds_dwordx4 v34, s[16:17] offset:2048 sc1 nt
	global_load_lds_dwordx4 v35, s[16:17] offset:3072 sc1 nt
	s_add_u32 s16, s16, 0x7d00
	s_addc_u32 s17, s17, 0
	v_cndmask_b32_e64 v30, 0, v30, s[18:19]
	v_cndmask_b32_e64 v31, 0, v31, s[18:19]
	v_cndmask_b32_e64 v32, 0, v32, s[18:19]
	v_cndmask_b32_e64 v33, 0, v33, s[18:19]
	v_max3_f32 v41, |v18|, |v19|, |v20|
	v_max3_f32 v42, |v21|, |v22|, |v23|
	v_max3_f32 v43, |v24|, |v25|, |v26|
	v_max3_f32 v44, |v27|, |v28|, |v29|
	v_max3_f32 v48, |v30|, |v31|, |v32|
	v_max3_f32 v41, v41, v42, |v33|
	v_max3_f32 v43, v43, v44, v48
	v_max_f32_e32 v41, v41, v43
	v_pk_add_f32 v[2:3], v[2:3], v[18:19]
	v_pk_add_f32 v[4:5], v[4:5], v[20:21]
	v_max_f32_dpp v41, v41, v41 quad_perm:[1,0,3,2] row_mask:0xf bank_mask:0xf
	v_pk_add_f32 v[6:7], v[6:7], v[22:23]
	v_pk_add_f32 v[8:9], v[8:9], v[24:25]
	v_max_f32_dpp v41, v41, v41 quad_perm:[2,3,0,1] row_mask:0xf bank_mask:0xf
	v_pk_add_f32 v[10:11], v[10:11], v[26:27]
	v_pk_add_f32 v[12:13], v[12:13], v[28:29]
	v_max_f32_dpp v41, v41, v41 row_half_mirror row_mask:0xf bank_mask:0xf
	v_pk_add_f32 v[14:15], v[14:15], v[30:31]
	v_pk_add_f32 v[16:17], v[16:17], v[32:33]
	v_max_f32_dpp v41, v41, v41 row_mirror row_mask:0xf bank_mask:0xf
	s_nop 1
	v_max_f32_dpp v41, v41, v41 row_bcast:15 row_mask:0xa bank_mask:0xf
	s_nop 1
	v_max_f32_dpp v41, v41, v41 row_bcast:31 row_mask:0xc bank_mask:0xf
	s_nop 1
	v_readlane_b32 s28, v41, 63
	s_nop 1
	v_div_scale_f32 v48, s[30:31], s28, s28, v47
	v_rcp_f32_e32 v49, v48
	s_nop 0
	v_fma_f32 v50, -v48, v49, 1.0
	v_fmac_f32_e32 v49, v50, v49
	v_mov_b32_e32 v50, s28
	v_div_scale_f32 v50, vcc, s32, v50, s32
	v_mul_f32_e32 v51, v50, v49
	v_fma_f32 v52, -v48, v51, v50
	v_fmac_f32_e32 v51, v52, v49
	v_fma_f32 v48, -v48, v51, v50
	v_div_fmas_f32 v48, v48, v49, v51
	v_div_fixup_f32 v48, v48, s28, v47
	v_cmp_gt_f32_e64 vcc, s28, 0
	v_writelane_b32 v40, s28, 18
	s_nop 0
	v_cndmask_b32_e32 v48, 0, v48, vcc
	v_fmaak_f32 v49, v18, v48, 0x4b400000
	v_fmaak_f32 v50, v19, v48, 0x4b400000
	v_fmaak_f32 v51, v20, v48, 0x4b400000
	v_fmaak_f32 v52, v21, v48, 0x4b400000
	v_perm_b32 v49, v50, v49, s33
	v_perm_b32 v51, v52, v51, s34
	v_or_b32_e32 v49, v49, v51
	s_add_u32 s20, s20, 0x4800
	s_addc_u32 s21, s21, 0
	s_add_u32 s22, s22, 0x4800
	s_addc_u32 s23, s23, 0
	s_add_u32 s24, s24, 0x4800
	s_addc_u32 s25, s25, 0
	s_add_u32 s26, s26, 0x4800
	s_addc_u32 s27, s27, 0
	global_store_dword v39, v49, s[20:21]
	v_fmaak_f32 v41, v22, v48, 0x4b400000
	v_fmaak_f32 v42, v23, v48, 0x4b400000
	v_fmaak_f32 v43, v24, v48, 0x4b400000
	v_fmaak_f32 v44, v25, v48, 0x4b400000
	v_perm_b32 v41, v42, v41, s33
	v_perm_b32 v43, v44, v43, s34
	v_or_b32_e32 v41, v41, v43
	global_store_dword v39, v41, s[22:23]
	v_fmaak_f32 v49, v26, v48, 0x4b400000
	v_fmaak_f32 v50, v27, v48, 0x4b400000
	v_fmaak_f32 v51, v28, v48, 0x4b400000
	v_fmaak_f32 v52, v29, v48, 0x4b400000
	v_perm_b32 v49, v50, v49, s33
	v_perm_b32 v51, v52, v51, s34
	v_or_b32_e32 v49, v49, v51
	global_store_dword v39, v49, s[24:25]
	v_fmaak_f32 v41, v30, v48, 0x4b400000
	v_fmaak_f32 v42, v31, v48, 0x4b400000
	v_fmaak_f32 v43, v32, v48, 0x4b400000
	v_fmaak_f32 v44, v33, v48, 0x4b400000
	v_perm_b32 v41, v42, v41, s33
	v_perm_b32 v43, v44, v43, s34
	v_or_b32_e32 v41, v41, v43
	global_store_dword v39, v41, s[26:27]
	s_waitcnt vmcnt(4)
	ds_read_b128 v[18:21], v38 offset:4096
	ds_read_b128 v[22:25], v38 offset:5120
	ds_read_b128 v[26:29], v38 offset:6144
	ds_read_b128 v[30:33], v38 offset:7168
	s_waitcnt lgkmcnt(0)
	s_mov_b32 m0, s35
	s_nop 0
	global_load_lds_dwordx4 v34, s[16:17] sc1 nt
	global_load_lds_dwordx4 v34, s[16:17] offset:1024 sc1 nt
	global_load_lds_dwordx4 v34, s[16:17] offset:2048 sc1 nt
	global_load_lds_dwordx4 v35, s[16:17] offset:3072 sc1 nt
	s_add_u32 s16, s16, 0x7d00
	s_addc_u32 s17, s17, 0
	v_cndmask_b32_e64 v30, 0, v30, s[18:19]
	v_cndmask_b32_e64 v31, 0, v31, s[18:19]
	v_cndmask_b32_e64 v32, 0, v32, s[18:19]
	v_cndmask_b32_e64 v33, 0, v33, s[18:19]
	v_max3_f32 v41, |v18|, |v19|, |v20|
	v_max3_f32 v42, |v21|, |v22|, |v23|
	v_max3_f32 v43, |v24|, |v25|, |v26|
	v_max3_f32 v44, |v27|, |v28|, |v29|
	v_max3_f32 v48, |v30|, |v31|, |v32|
	v_max3_f32 v41, v41, v42, |v33|
	v_max3_f32 v43, v43, v44, v48
	v_max_f32_e32 v41, v41, v43
	v_pk_add_f32 v[2:3], v[2:3], v[18:19]
	v_pk_add_f32 v[4:5], v[4:5], v[20:21]
	v_max_f32_dpp v41, v41, v41 quad_perm:[1,0,3,2] row_mask:0xf bank_mask:0xf
	v_pk_add_f32 v[6:7], v[6:7], v[22:23]
	v_pk_add_f32 v[8:9], v[8:9], v[24:25]
	v_max_f32_dpp v41, v41, v41 quad_perm:[2,3,0,1] row_mask:0xf bank_mask:0xf
	v_pk_add_f32 v[10:11], v[10:11], v[26:27]
	v_pk_add_f32 v[12:13], v[12:13], v[28:29]
	v_max_f32_dpp v41, v41, v41 row_half_mirror row_mask:0xf bank_mask:0xf
	v_pk_add_f32 v[14:15], v[14:15], v[30:31]
	v_pk_add_f32 v[16:17], v[16:17], v[32:33]
	v_max_f32_dpp v41, v41, v41 row_mirror row_mask:0xf bank_mask:0xf
	s_nop 1
	v_max_f32_dpp v41, v41, v41 row_bcast:15 row_mask:0xa bank_mask:0xf
	s_nop 1
	v_max_f32_dpp v41, v41, v41 row_bcast:31 row_mask:0xc bank_mask:0xf
	s_nop 1
	v_readlane_b32 s28, v41, 63
	s_nop 1
	v_div_scale_f32 v48, s[30:31], s28, s28, v47
	v_rcp_f32_e32 v49, v48
	s_nop 0
	v_fma_f32 v50, -v48, v49, 1.0
	v_fmac_f32_e32 v49, v50, v49
	v_mov_b32_e32 v50, s28
	v_div_scale_f32 v50, vcc, s32, v50, s32
	v_mul_f32_e32 v51, v50, v49
	v_fma_f32 v52, -v48, v51, v50
	v_fmac_f32_e32 v51, v52, v49
	v_fma_f32 v48, -v48, v51, v50
	v_div_fmas_f32 v48, v48, v49, v51
	v_div_fixup_f32 v48, v48, s28, v47
	v_cmp_gt_f32_e64 vcc, s28, 0
	v_writelane_b32 v40, s28, 19
	s_nop 0
	v_cndmask_b32_e32 v48, 0, v48, vcc
	v_fmaak_f32 v49, v18, v48, 0x4b400000
	v_fmaak_f32 v50, v19, v48, 0x4b400000
	v_fmaak_f32 v51, v20, v48, 0x4b400000
	v_fmaak_f32 v52, v21, v48, 0x4b400000
	v_perm_b32 v49, v50, v49, s33
	v_perm_b32 v51, v52, v51, s34
	v_or_b32_e32 v49, v49, v51
	s_add_u32 s20, s20, 0x400
	s_addc_u32 s21, s21, 0
	s_add_u32 s22, s22, 0x400
	s_addc_u32 s23, s23, 0
	s_add_u32 s24, s24, 0x400
	s_addc_u32 s25, s25, 0
	s_add_u32 s26, s26, 0x400
	s_addc_u32 s27, s27, 0
	global_store_dword v39, v49, s[20:21]
	v_fmaak_f32 v41, v22, v48, 0x4b400000
	v_fmaak_f32 v42, v23, v48, 0x4b400000
	v_fmaak_f32 v43, v24, v48, 0x4b400000
	v_fmaak_f32 v44, v25, v48, 0x4b400000
	v_perm_b32 v41, v42, v41, s33
	v_perm_b32 v43, v44, v43, s34
	v_or_b32_e32 v41, v41, v43
	global_store_dword v39, v41, s[22:23]
	v_fmaak_f32 v49, v26, v48, 0x4b400000
	v_fmaak_f32 v50, v27, v48, 0x4b400000
	v_fmaak_f32 v51, v28, v48, 0x4b400000
	v_fmaak_f32 v52, v29, v48, 0x4b400000
	v_perm_b32 v49, v50, v49, s33
	v_perm_b32 v51, v52, v51, s34
	v_or_b32_e32 v49, v49, v51
	global_store_dword v39, v49, s[24:25]
	v_fmaak_f32 v41, v30, v48, 0x4b400000
	v_fmaak_f32 v42, v31, v48, 0x4b400000
	v_fmaak_f32 v43, v32, v48, 0x4b400000
	v_fmaak_f32 v44, v33, v48, 0x4b400000
	v_perm_b32 v41, v42, v41, s33
	v_perm_b32 v43, v44, v43, s34
	v_or_b32_e32 v41, v41, v43
	global_store_dword v39, v41, s[26:27]
	s_waitcnt vmcnt(4)
	ds_read_b128 v[18:21], v38 offset:0
	ds_read_b128 v[22:25], v38 offset:1024
	ds_read_b128 v[26:29], v38 offset:2048
	ds_read_b128 v[30:33], v38 offset:3072
	s_waitcnt lgkmcnt(0)
	s_mov_b32 m0, s36
	s_nop 0
	global_load_lds_dwordx4 v34, s[16:17] sc1 nt
	global_load_lds_dwordx4 v34, s[16:17] offset:1024 sc1 nt
	global_load_lds_dwordx4 v34, s[16:17] offset:2048 sc1 nt
	global_load_lds_dwordx4 v35, s[16:17] offset:3072 sc1 nt
	s_add_u32 s16, s16, 0x7d00
	s_addc_u32 s17, s17, 0
	v_cndmask_b32_e64 v30, 0, v30, s[18:19]
	v_cndmask_b32_e64 v31, 0, v31, s[18:19]
	v_cndmask_b32_e64 v32, 0, v32, s[18:19]
	v_cndmask_b32_e64 v33, 0, v33, s[18:19]
	v_max3_f32 v41, |v18|, |v19|, |v20|
	v_max3_f32 v42, |v21|, |v22|, |v23|
	v_max3_f32 v43, |v24|, |v25|, |v26|
	v_max3_f32 v44, |v27|, |v28|, |v29|
	v_max3_f32 v48, |v30|, |v31|, |v32|
	v_max3_f32 v41, v41, v42, |v33|
	v_max3_f32 v43, v43, v44, v48
	v_max_f32_e32 v41, v41, v43
	v_pk_add_f32 v[2:3], v[2:3], v[18:19]
	v_pk_add_f32 v[4:5], v[4:5], v[20:21]
	v_max_f32_dpp v41, v41, v41 quad_perm:[1,0,3,2] row_mask:0xf bank_mask:0xf
	v_pk_add_f32 v[6:7], v[6:7], v[22:23]
	v_pk_add_f32 v[8:9], v[8:9], v[24:25]
	v_max_f32_dpp v41, v41, v41 quad_perm:[2,3,0,1] row_mask:0xf bank_mask:0xf
	v_pk_add_f32 v[10:11], v[10:11], v[26:27]
	v_pk_add_f32 v[12:13], v[12:13], v[28:29]
	v_max_f32_dpp v41, v41, v41 row_half_mirror row_mask:0xf bank_mask:0xf
	v_pk_add_f32 v[14:15], v[14:15], v[30:31]
	v_pk_add_f32 v[16:17], v[16:17], v[32:33]
	v_max_f32_dpp v41, v41, v41 row_mirror row_mask:0xf bank_mask:0xf
	s_nop 1
	v_max_f32_dpp v41, v41, v41 row_bcast:15 row_mask:0xa bank_mask:0xf
	s_nop 1
	v_max_f32_dpp v41, v41, v41 row_bcast:31 row_mask:0xc bank_mask:0xf
	s_nop 1
	v_readlane_b32 s28, v41, 63
	s_nop 1
	v_div_scale_f32 v48, s[30:31], s28, s28, v47
	v_rcp_f32_e32 v49, v48
	s_nop 0
	v_fma_f32 v50, -v48, v49, 1.0
	v_fmac_f32_e32 v49, v50, v49
	v_mov_b32_e32 v50, s28
	v_div_scale_f32 v50, vcc, s32, v50, s32
	v_mul_f32_e32 v51, v50, v49
	v_fma_f32 v52, -v48, v51, v50
	v_fmac_f32_e32 v51, v52, v49
	v_fma_f32 v48, -v48, v51, v50
	v_div_fmas_f32 v48, v48, v49, v51
	v_div_fixup_f32 v48, v48, s28, v47
	v_cmp_gt_f32_e64 vcc, s28, 0
	v_writelane_b32 v40, s28, 20
	s_nop 0
	v_cndmask_b32_e32 v48, 0, v48, vcc
	v_fmaak_f32 v49, v18, v48, 0x4b400000
	v_fmaak_f32 v50, v19, v48, 0x4b400000
	v_fmaak_f32 v51, v20, v48, 0x4b400000
	v_fmaak_f32 v52, v21, v48, 0x4b400000
	v_perm_b32 v49, v50, v49, s33
	v_perm_b32 v51, v52, v51, s34
	v_or_b32_e32 v49, v49, v51
	s_add_u32 s20, s20, 0x400
	s_addc_u32 s21, s21, 0
	s_add_u32 s22, s22, 0x400
	s_addc_u32 s23, s23, 0
	s_add_u32 s24, s24, 0x400
	s_addc_u32 s25, s25, 0
	s_add_u32 s26, s26, 0x400
	s_addc_u32 s27, s27, 0
	global_store_dword v39, v49, s[20:21]
	v_fmaak_f32 v41, v22, v48, 0x4b400000
	v_fmaak_f32 v42, v23, v48, 0x4b400000
	v_fmaak_f32 v43, v24, v48, 0x4b400000
	v_fmaak_f32 v44, v25, v48, 0x4b400000
	v_perm_b32 v41, v42, v41, s33
	v_perm_b32 v43, v44, v43, s34
	v_or_b32_e32 v41, v41, v43
	global_store_dword v39, v41, s[22:23]
	v_fmaak_f32 v49, v26, v48, 0x4b400000
	v_fmaak_f32 v50, v27, v48, 0x4b400000
	v_fmaak_f32 v51, v28, v48, 0x4b400000
	v_fmaak_f32 v52, v29, v48, 0x4b400000
	v_perm_b32 v49, v50, v49, s33
	v_perm_b32 v51, v52, v51, s34
	v_or_b32_e32 v49, v49, v51
	global_store_dword v39, v49, s[24:25]
	v_fmaak_f32 v41, v30, v48, 0x4b400000
	v_fmaak_f32 v42, v31, v48, 0x4b400000
	v_fmaak_f32 v43, v32, v48, 0x4b400000
	v_fmaak_f32 v44, v33, v48, 0x4b400000
	v_perm_b32 v41, v42, v41, s33
	v_perm_b32 v43, v44, v43, s34
	v_or_b32_e32 v41, v41, v43
	global_store_dword v39, v41, s[26:27]
	s_waitcnt vmcnt(4)
	ds_read_b128 v[18:21], v38 offset:4096
	ds_read_b128 v[22:25], v38 offset:5120
	ds_read_b128 v[26:29], v38 offset:6144
	ds_read_b128 v[30:33], v38 offset:7168
	s_waitcnt lgkmcnt(0)
	s_mov_b32 m0, s35
	s_nop 0
	global_load_lds_dwordx4 v34, s[16:17] sc1 nt
	global_load_lds_dwordx4 v34, s[16:17] offset:1024 sc1 nt
	global_load_lds_dwordx4 v34, s[16:17] offset:2048 sc1 nt
	global_load_lds_dwordx4 v35, s[16:17] offset:3072 sc1 nt
	s_add_u32 s16, s16, 0x7d00
	s_addc_u32 s17, s17, 0
	v_cndmask_b32_e64 v30, 0, v30, s[18:19]
	v_cndmask_b32_e64 v31, 0, v31, s[18:19]
	v_cndmask_b32_e64 v32, 0, v32, s[18:19]
	v_cndmask_b32_e64 v33, 0, v33, s[18:19]
	v_max3_f32 v41, |v18|, |v19|, |v20|
	v_max3_f32 v42, |v21|, |v22|, |v23|
	v_max3_f32 v43, |v24|, |v25|, |v26|
	v_max3_f32 v44, |v27|, |v28|, |v29|
	v_max3_f32 v48, |v30|, |v31|, |v32|
	v_max3_f32 v41, v41, v42, |v33|
	v_max3_f32 v43, v43, v44, v48
	v_max_f32_e32 v41, v41, v43
	v_pk_add_f32 v[2:3], v[2:3], v[18:19]
	v_pk_add_f32 v[4:5], v[4:5], v[20:21]
	v_max_f32_dpp v41, v41, v41 quad_perm:[1,0,3,2] row_mask:0xf bank_mask:0xf
	v_pk_add_f32 v[6:7], v[6:7], v[22:23]
	v_pk_add_f32 v[8:9], v[8:9], v[24:25]
	v_max_f32_dpp v41, v41, v41 quad_perm:[2,3,0,1] row_mask:0xf bank_mask:0xf
	v_pk_add_f32 v[10:11], v[10:11], v[26:27]
	v_pk_add_f32 v[12:13], v[12:13], v[28:29]
	v_max_f32_dpp v41, v41, v41 row_half_mirror row_mask:0xf bank_mask:0xf
	v_pk_add_f32 v[14:15], v[14:15], v[30:31]
	v_pk_add_f32 v[16:17], v[16:17], v[32:33]
	v_max_f32_dpp v41, v41, v41 row_mirror row_mask:0xf bank_mask:0xf
	s_nop 1
	v_max_f32_dpp v41, v41, v41 row_bcast:15 row_mask:0xa bank_mask:0xf
	s_nop 1
	v_max_f32_dpp v41, v41, v41 row_bcast:31 row_mask:0xc bank_mask:0xf
	s_nop 1
	v_readlane_b32 s28, v41, 63
	s_nop 1
	v_div_scale_f32 v48, s[30:31], s28, s28, v47
	v_rcp_f32_e32 v49, v48
	s_nop 0
	v_fma_f32 v50, -v48, v49, 1.0
	v_fmac_f32_e32 v49, v50, v49
	v_mov_b32_e32 v50, s28
	v_div_scale_f32 v50, vcc, s32, v50, s32
	v_mul_f32_e32 v51, v50, v49
	v_fma_f32 v52, -v48, v51, v50
	v_fmac_f32_e32 v51, v52, v49
	v_fma_f32 v48, -v48, v51, v50
	v_div_fmas_f32 v48, v48, v49, v51
	v_div_fixup_f32 v48, v48, s28, v47
	v_cmp_gt_f32_e64 vcc, s28, 0
	v_writelane_b32 v40, s28, 21
	s_nop 0
	v_cndmask_b32_e32 v48, 0, v48, vcc
	v_fmaak_f32 v49, v18, v48, 0x4b400000
	v_fmaak_f32 v50, v19, v48, 0x4b400000
	v_fmaak_f32 v51, v20, v48, 0x4b400000
	v_fmaak_f32 v52, v21, v48, 0x4b400000
	v_perm_b32 v49, v50, v49, s33
	v_perm_b32 v51, v52, v51, s34
	v_or_b32_e32 v49, v49, v51
	s_add_u32 s20, s20, 0x400
	s_addc_u32 s21, s21, 0
	s_add_u32 s22, s22, 0x400
	s_addc_u32 s23, s23, 0
	s_add_u32 s24, s24, 0x400
	s_addc_u32 s25, s25, 0
	s_add_u32 s26, s26, 0x400
	s_addc_u32 s27, s27, 0
	global_store_dword v39, v49, s[20:21]
	v_fmaak_f32 v41, v22, v48, 0x4b400000
	v_fmaak_f32 v42, v23, v48, 0x4b400000
	v_fmaak_f32 v43, v24, v48, 0x4b400000
	v_fmaak_f32 v44, v25, v48, 0x4b400000
	v_perm_b32 v41, v42, v41, s33
	v_perm_b32 v43, v44, v43, s34
	v_or_b32_e32 v41, v41, v43
	global_store_dword v39, v41, s[22:23]
	v_fmaak_f32 v49, v26, v48, 0x4b400000
	v_fmaak_f32 v50, v27, v48, 0x4b400000
	v_fmaak_f32 v51, v28, v48, 0x4b400000
	v_fmaak_f32 v52, v29, v48, 0x4b400000
	v_perm_b32 v49, v50, v49, s33
	v_perm_b32 v51, v52, v51, s34
	v_or_b32_e32 v49, v49, v51
	global_store_dword v39, v49, s[24:25]
	v_fmaak_f32 v41, v30, v48, 0x4b400000
	v_fmaak_f32 v42, v31, v48, 0x4b400000
	v_fmaak_f32 v43, v32, v48, 0x4b400000
	v_fmaak_f32 v44, v33, v48, 0x4b400000
	v_perm_b32 v41, v42, v41, s33
	v_perm_b32 v43, v44, v43, s34
	v_or_b32_e32 v41, v41, v43
	global_store_dword v39, v41, s[26:27]
	s_waitcnt vmcnt(4)
	ds_read_b128 v[18:21], v38 offset:0
	ds_read_b128 v[22:25], v38 offset:1024
	ds_read_b128 v[26:29], v38 offset:2048
	ds_read_b128 v[30:33], v38 offset:3072
	s_waitcnt lgkmcnt(0)
	s_mov_b32 m0, s36
	s_nop 0
	global_load_lds_dwordx4 v34, s[16:17] sc1 nt
	global_load_lds_dwordx4 v34, s[16:17] offset:1024 sc1 nt
	global_load_lds_dwordx4 v34, s[16:17] offset:2048 sc1 nt
	global_load_lds_dwordx4 v35, s[16:17] offset:3072 sc1 nt
	s_add_u32 s16, s16, 0x7d00
	s_addc_u32 s17, s17, 0
	v_cndmask_b32_e64 v30, 0, v30, s[18:19]
	v_cndmask_b32_e64 v31, 0, v31, s[18:19]
	v_cndmask_b32_e64 v32, 0, v32, s[18:19]
	v_cndmask_b32_e64 v33, 0, v33, s[18:19]
	v_max3_f32 v41, |v18|, |v19|, |v20|
	v_max3_f32 v42, |v21|, |v22|, |v23|
	v_max3_f32 v43, |v24|, |v25|, |v26|
	v_max3_f32 v44, |v27|, |v28|, |v29|
	v_max3_f32 v48, |v30|, |v31|, |v32|
	v_max3_f32 v41, v41, v42, |v33|
	v_max3_f32 v43, v43, v44, v48
	v_max_f32_e32 v41, v41, v43
	v_pk_add_f32 v[2:3], v[2:3], v[18:19]
	v_pk_add_f32 v[4:5], v[4:5], v[20:21]
	v_max_f32_dpp v41, v41, v41 quad_perm:[1,0,3,2] row_mask:0xf bank_mask:0xf
	v_pk_add_f32 v[6:7], v[6:7], v[22:23]
	v_pk_add_f32 v[8:9], v[8:9], v[24:25]
	v_max_f32_dpp v41, v41, v41 quad_perm:[2,3,0,1] row_mask:0xf bank_mask:0xf
	v_pk_add_f32 v[10:11], v[10:11], v[26:27]
	v_pk_add_f32 v[12:13], v[12:13], v[28:29]
	v_max_f32_dpp v41, v41, v41 row_half_mirror row_mask:0xf bank_mask:0xf
	v_pk_add_f32 v[14:15], v[14:15], v[30:31]
	v_pk_add_f32 v[16:17], v[16:17], v[32:33]
	v_max_f32_dpp v41, v41, v41 row_mirror row_mask:0xf bank_mask:0xf
	s_nop 1
	v_max_f32_dpp v41, v41, v41 row_bcast:15 row_mask:0xa bank_mask:0xf
	s_nop 1
	v_max_f32_dpp v41, v41, v41 row_bcast:31 row_mask:0xc bank_mask:0xf
	s_nop 1
	v_readlane_b32 s28, v41, 63
	s_nop 1
	v_div_scale_f32 v48, s[30:31], s28, s28, v47
	v_rcp_f32_e32 v49, v48
	s_nop 0
	v_fma_f32 v50, -v48, v49, 1.0
	v_fmac_f32_e32 v49, v50, v49
	v_mov_b32_e32 v50, s28
	v_div_scale_f32 v50, vcc, s32, v50, s32
	v_mul_f32_e32 v51, v50, v49
	v_fma_f32 v52, -v48, v51, v50
	v_fmac_f32_e32 v51, v52, v49
	v_fma_f32 v48, -v48, v51, v50
	v_div_fmas_f32 v48, v48, v49, v51
	v_div_fixup_f32 v48, v48, s28, v47
	v_cmp_gt_f32_e64 vcc, s28, 0
	v_writelane_b32 v40, s28, 22
	s_nop 0
	v_cndmask_b32_e32 v48, 0, v48, vcc
	v_fmaak_f32 v49, v18, v48, 0x4b400000
	v_fmaak_f32 v50, v19, v48, 0x4b400000
	v_fmaak_f32 v51, v20, v48, 0x4b400000
	v_fmaak_f32 v52, v21, v48, 0x4b400000
	v_perm_b32 v49, v50, v49, s33
	v_perm_b32 v51, v52, v51, s34
	v_or_b32_e32 v49, v49, v51
	s_add_u32 s20, s20, 0x400
	s_addc_u32 s21, s21, 0
	s_add_u32 s22, s22, 0x400
	s_addc_u32 s23, s23, 0
	s_add_u32 s24, s24, 0x400
	s_addc_u32 s25, s25, 0
	s_add_u32 s26, s26, 0x400
	s_addc_u32 s27, s27, 0
	global_store_dword v39, v49, s[20:21]
	v_fmaak_f32 v41, v22, v48, 0x4b400000
	v_fmaak_f32 v42, v23, v48, 0x4b400000
	v_fmaak_f32 v43, v24, v48, 0x4b400000
	v_fmaak_f32 v44, v25, v48, 0x4b400000
	v_perm_b32 v41, v42, v41, s33
	v_perm_b32 v43, v44, v43, s34
	v_or_b32_e32 v41, v41, v43
	global_store_dword v39, v41, s[22:23]
	v_fmaak_f32 v49, v26, v48, 0x4b400000
	v_fmaak_f32 v50, v27, v48, 0x4b400000
	v_fmaak_f32 v51, v28, v48, 0x4b400000
	v_fmaak_f32 v52, v29, v48, 0x4b400000
	v_perm_b32 v49, v50, v49, s33
	v_perm_b32 v51, v52, v51, s34
	v_or_b32_e32 v49, v49, v51
	global_store_dword v39, v49, s[24:25]
	v_fmaak_f32 v41, v30, v48, 0x4b400000
	v_fmaak_f32 v42, v31, v48, 0x4b400000
	v_fmaak_f32 v43, v32, v48, 0x4b400000
	v_fmaak_f32 v44, v33, v48, 0x4b400000
	v_perm_b32 v41, v42, v41, s33
	v_perm_b32 v43, v44, v43, s34
	v_or_b32_e32 v41, v41, v43
	global_store_dword v39, v41, s[26:27]
	s_waitcnt vmcnt(4)
	ds_read_b128 v[18:21], v38 offset:4096
	ds_read_b128 v[22:25], v38 offset:5120
	ds_read_b128 v[26:29], v38 offset:6144
	ds_read_b128 v[30:33], v38 offset:7168
	s_waitcnt lgkmcnt(0)
	s_cmp_eq_u32 s29, 1
	s_cbranch_scc0 .Lk1_nodma24
	s_mov_b32 m0, s35
	s_nop 0
	global_load_lds_dwordx4 v34, s[16:17] sc1 nt
	global_load_lds_dwordx4 v34, s[16:17] offset:1024 sc1 nt
	global_load_lds_dwordx4 v34, s[16:17] offset:2048 sc1 nt
	global_load_lds_dwordx4 v35, s[16:17] offset:3072 sc1 nt
	s_add_u32 s16, s16, 0x7d00
	s_addc_u32 s17, s17, 0
